# P1: x rows read non-temporal (on top of non-temporal PROJ stores)
# speedup vs baseline: 1.0186x; 1.0186x over previous
.LBB0_1022:
	global_load_dwordx4 v[30:33], v[78:79], off offset:-4096
	global_load_dwordx4 v[26:29], v[78:79], off offset:-3072
	global_load_dwordx4 v[22:25], v[78:79], off offset:-2048
	global_load_dwordx4 v[18:21], v[78:79], off offset:-1024
	global_load_dwordx4 v[14:17], v[78:79], off nt
	global_load_dwordx4 v[10:13], v[78:79], off offset:1024 nt
	global_load_dwordx4 v[6:9], v[78:79], off offset:2048 nt
	global_load_dwordx4 v[2:5], v[78:79], off offset:3072 nt
	s_lshr_b32 s14, s13, 11
	s_mulk_i32 s14, 0x3000
	s_ashr_i32 s15, s14, 31
	s_lshl_b64 s[14:15], s[14:15], 2
	s_add_u32 s14, s2, s14
	global_load_dwordx4 v[34:37], v[66:67], off nt
	global_load_dwordx4 v[38:41], v[66:67], off offset:1024 nt
	global_load_dwordx4 v[42:45], v[66:67], off offset:2048 nt
	global_load_dwordx4 v[46:49], v[66:67], off offset:3072 nt
	global_load_dwordx4 v[50:53], v[68:69], off nt
	global_load_dwordx4 v[54:57], v[70:71], off nt
	global_load_dwordx4 v[58:61], v[72:73], off nt
	global_load_dwordx4 v[62:65], v[74:75], off nt
	s_addc_u32 s15, s3, s15
	s_add_u32 s16, s14, 0x2000
	s_addc_u32 s17, s15, 0
	global_load_dwordx4 v[96:99], v86, s[14:15]
	global_load_dwordx4 v[100:103], v86, s[14:15] offset:1024
	global_load_dwordx4 v[104:107], v86, s[14:15] offset:2048
	global_load_dwordx4 v[108:111], v86, s[14:15] offset:3072
	global_load_dwordx4 v[112:115], v86, s[16:17]
	global_load_dwordx4 v[116:119], v87, s[16:17]
	global_load_dwordx4 v[120:123], v88, s[16:17]
	global_load_dwordx4 v[124:127], v89, s[16:17]
	global_load_dwordx4 v[128:131], v90, s[16:17]
	global_load_dwordx4 v[132:135], v91, s[16:17]
	global_load_dwordx4 v[136:139], v92, s[16:17]
	global_load_dwordx4 v[140:143], v93, s[16:17]
	global_load_dwordx4 v[144:147], v90, s[14:15]
	global_load_dwordx4 v[148:151], v91, s[14:15]
	global_load_dwordx4 v[152:155], v92, s[14:15]
	global_load_dwordx4 v[156:159], v93, s[14:15]
	v_mov_b32_e32 v183, 0
	v_mov_b32_e32 v186, 0
	v_mov_b32_e32 v187, 0
	v_mov_b32_e32 v188, 0
	v_mov_b32_e32 v189, 0
	v_mov_b32_e32 v190, 0
	v_mov_b32_e32 v191, 0
	v_mov_b32_e32 v192, 0
	s_add_i32 s13, s13, s20
	v_lshl_add_u64 v[78:79], v[78:79], 0, s[10:11]
	s_cmpk_lt_i32 s13, 0x4000
	s_waitcnt vmcnt(31)
	v_mov_b32_e32 v162, v31
	s_waitcnt vmcnt(30)
	v_mov_b32_e32 v163, v27
	v_mov_b32_e32 v166, v33
	v_mov_b32_e32 v167, v29
	v_mov_b32_e32 v160, v30
	v_mov_b32_e32 v161, v26
	v_mov_b32_e32 v164, v32
	v_mov_b32_e32 v165, v28
	s_waitcnt vmcnt(29)
	v_pk_mul_f32 v[168:169], v[24:25], v[24:25]
	v_pk_mul_f32 v[170:171], v[22:23], v[22:23]
	v_pk_mul_f32 v[162:163], v[162:163], v[162:163]
	v_pk_mul_f32 v[166:167], v[166:167], v[166:167]
	v_pk_mov_b32 v[184:185], v[170:171], v[168:169] op_sel:[1,0]
	v_mov_b32_e32 v171, v169
	v_pk_fma_f32 v[160:161], v[160:161], v[160:161], v[162:163]
	v_pk_fma_f32 v[162:163], v[164:165], v[164:165], v[166:167]
	s_waitcnt vmcnt(28)
	v_mul_f32_e32 v172, v18, v18
	v_mul_f32_e32 v174, v20, v20
	v_pk_add_f32 v[164:165], v[184:185], v[170:171]
	v_pk_add_f32 v[160:161], v[160:161], v[162:163]
	v_pk_fma_f32 v[168:169], v[18:19], v[18:19], v[172:173] op_sel_hi:[1,1,0]
	v_pk_fma_f32 v[172:173], v[20:21], v[20:21], v[174:175] op_sel_hi:[1,1,0]
	v_pk_add_f32 v[162:163], v[164:165], v[164:165] op_sel_hi:[0,1]
	v_pk_add_f32 v[160:161], v[160:161], v[160:161] op_sel_hi:[0,1]
	s_waitcnt vmcnt(26)
	v_pk_mul_f32 v[176:177], v[12:13], v[12:13]
	v_pk_mul_f32 v[178:179], v[10:11], v[10:11]
	v_mul_f32_e32 v168, v14, v14
	v_mul_f32_e32 v172, v15, v15
	v_mul_f32_e32 v162, v16, v16
	v_mul_f32_e32 v160, v17, v17
	v_pk_mov_b32 v[174:175], v[178:179], v[176:177] op_sel:[1,0]
	v_mov_b32_e32 v179, v177
	v_pk_add_f32 v[164:165], v[168:169], v[172:173]
	v_pk_add_f32 v[160:161], v[162:163], v[160:161]
	s_waitcnt vmcnt(25)
	v_mul_f32_e32 v180, v6, v6
	v_mul_f32_e32 v182, v8, v8
	v_pk_add_f32 v[166:167], v[174:175], v[178:179]
	v_pk_add_f32 v[160:161], v[164:165], v[160:161]
	v_pk_fma_f32 v[176:177], v[6:7], v[6:7], v[180:181] op_sel_hi:[1,1,0]
	v_pk_fma_f32 v[180:181], v[8:9], v[8:9], v[182:183] op_sel_hi:[1,1,0]
	v_pk_add_f32 v[166:167], v[166:167], v[166:167] op_sel_hi:[0,1]
	v_pk_add_f32 v[160:161], v[160:161], v[160:161] op_sel_hi:[0,1]
	s_waitcnt vmcnt(24)
	v_mul_f32_e32 v176, v2, v2
	v_mul_f32_e32 v180, v3, v3
	v_mul_f32_e32 v166, v4, v4
	s_waitcnt vmcnt(11)
	v_pk_add_f32 v[112:113], v[112:113], 1.0 op_sel_hi:[1,0]
	v_mul_f32_e32 v160, v5, v5
	v_pk_add_f32 v[168:169], v[176:177], v[180:181]
	v_pk_mul_f32 v[34:35], v[34:35], v[112:113]
	v_pk_add_f32 v[112:113], v[166:167], v[160:161]
	s_waitcnt vmcnt(10)
	v_pk_add_f32 v[116:117], v[116:117], 1.0 op_sel_hi:[1,0]
	v_pk_add_f32 v[112:113], v[168:169], v[112:113]
	s_waitcnt vmcnt(9)
	v_pk_add_f32 v[120:121], v[120:121], 1.0 op_sel_hi:[1,0]
	v_add_f32_e32 v112, v112, v113
	ds_bpermute_b32 v113, v1, v112
	v_pk_mul_f32 v[38:39], v[38:39], v[116:117]
	s_waitcnt vmcnt(8)
	v_pk_add_f32 v[124:125], v[124:125], 1.0 op_sel_hi:[1,0]
	v_pk_mul_f32 v[42:43], v[42:43], v[120:121]
	v_pk_add_f32 v[114:115], v[114:115], 1.0 op_sel_hi:[1,0]
	s_waitcnt lgkmcnt(0)
	v_add_f32_e32 v112, v112, v113
	ds_bpermute_b32 v113, v81, v112
	s_waitcnt vmcnt(7)
	v_pk_add_f32 v[128:129], v[128:129], 1.0 op_sel_hi:[1,0]
	s_waitcnt vmcnt(6)
	v_pk_add_f32 v[132:133], v[132:133], 1.0 op_sel_hi:[1,0]
	s_waitcnt vmcnt(5)
	v_pk_add_f32 v[136:137], v[136:137], 1.0 op_sel_hi:[1,0]
	s_waitcnt vmcnt(4)
	v_pk_add_f32 v[140:141], v[140:141], 1.0 op_sel_hi:[1,0]
	s_waitcnt lgkmcnt(0)
	v_add_f32_e32 v112, v112, v113
	ds_bpermute_b32 v113, v82, v112
	v_pk_mul_f32 v[46:47], v[46:47], v[124:125]
	v_pk_add_f32 v[118:119], v[118:119], 1.0 op_sel_hi:[1,0]
	v_pk_mul_f32 v[36:37], v[36:37], v[114:115]
	v_pk_mul_f32 v[50:51], v[50:51], v[128:129]
	s_waitcnt lgkmcnt(0)
	v_add_f32_e32 v112, v112, v113
	ds_bpermute_b32 v113, v83, v112
	v_pk_mul_f32 v[54:55], v[54:55], v[132:133]
	v_pk_mul_f32 v[58:59], v[58:59], v[136:137]
	v_pk_mul_f32 v[62:63], v[62:63], v[140:141]
	v_pk_add_f32 v[122:123], v[122:123], 1.0 op_sel_hi:[1,0]
	s_waitcnt lgkmcnt(0)
	v_add_f32_e32 v112, v112, v113
	ds_bpermute_b32 v113, v84, v112
	v_pk_mul_f32 v[40:41], v[40:41], v[118:119]
	v_pk_add_f32 v[126:127], v[126:127], 1.0 op_sel_hi:[1,0]
	v_pk_mul_f32 v[44:45], v[44:45], v[122:123]
	v_pk_add_f32 v[130:131], v[130:131], 1.0 op_sel_hi:[1,0]
	s_waitcnt lgkmcnt(0)
	v_add_f32_e32 v112, v112, v113
	ds_bpermute_b32 v113, v85, v112
	v_pk_add_f32 v[134:135], v[134:135], 1.0 op_sel_hi:[1,0]
	v_pk_add_f32 v[138:139], v[138:139], 1.0 op_sel_hi:[1,0]
	v_pk_add_f32 v[142:143], v[142:143], 1.0 op_sel_hi:[1,0]
	v_pk_mul_f32 v[48:49], v[48:49], v[126:127]
	s_waitcnt lgkmcnt(0)
	v_add_f32_e32 v112, v112, v113
	v_fmamk_f32 v112, v112, 0x3a000000, v94
	v_mul_f32_e32 v113, 0x4b800000, v112
	v_cmp_gt_f32_e32 vcc, s1, v112
	v_pk_mul_f32 v[52:53], v[52:53], v[130:131]
	v_pk_mul_f32 v[56:57], v[56:57], v[134:135]
	v_cndmask_b32_e32 v112, v112, v113, vcc
	v_rsq_f32_e32 v112, v112
	v_pk_mul_f32 v[60:61], v[60:61], v[138:139]
	v_pk_mul_f32 v[64:65], v[64:65], v[142:143]
	v_mul_f32_e32 v113, 0x45800000, v112
	v_cndmask_b32_e32 v112, v112, v113, vcc
	v_pk_mul_f32 v[30:31], v[30:31], v[112:113] op_sel_hi:[1,0]
	v_pk_mul_f32 v[26:27], v[26:27], v[112:113] op_sel_hi:[1,0]
	v_pk_fma_f32 v[30:31], v[34:35], v[30:31], v[96:97]
	v_pk_mul_f32 v[22:23], v[22:23], v[112:113] op_sel_hi:[1,0]
	v_pk_fma_f32 v[26:27], v[38:39], v[26:27], v[100:101]
	v_med3_f32 v30, v30, s12, v95
	v_med3_f32 v31, v31, s12, v95
	v_pk_mul_f32 v[18:19], v[18:19], v[112:113] op_sel_hi:[1,0]
	v_pk_fma_f32 v[22:23], v[42:43], v[22:23], v[104:105]
	v_med3_f32 v26, v26, s12, v95
	v_med3_f32 v27, v27, s12, v95
	v_cvt_pk_fp8_f32 v183, v30, v31
	v_pk_mul_f32 v[32:33], v[32:33], v[112:113] op_sel_hi:[1,0]
	v_pk_mul_f32 v[14:15], v[14:15], v[112:113] op_sel_hi:[1,0]
	v_pk_mul_f32 v[10:11], v[10:11], v[112:113] op_sel_hi:[1,0]
	v_pk_mul_f32 v[6:7], v[6:7], v[112:113] op_sel_hi:[1,0]
	v_pk_mul_f32 v[2:3], v[2:3], v[112:113] op_sel_hi:[1,0]
	v_pk_fma_f32 v[18:19], v[46:47], v[18:19], v[108:109]
	v_med3_f32 v22, v22, s12, v95
	v_med3_f32 v23, v23, s12, v95
	v_cvt_pk_fp8_f32 v186, v26, v27
	v_pk_mul_f32 v[28:29], v[28:29], v[112:113] op_sel_hi:[1,0]
	v_pk_fma_f32 v[32:33], v[36:37], v[32:33], v[98:99]
	s_waitcnt vmcnt(3)
	v_pk_fma_f32 v[14:15], v[50:51], v[14:15], v[144:145]
	s_waitcnt vmcnt(2)
	v_pk_fma_f32 v[10:11], v[54:55], v[10:11], v[148:149]
	s_waitcnt vmcnt(1)
	v_pk_fma_f32 v[6:7], v[58:59], v[6:7], v[152:153]
	s_waitcnt vmcnt(0)
	v_pk_fma_f32 v[2:3], v[62:63], v[2:3], v[156:157]
	v_med3_f32 v18, v18, s12, v95
	v_med3_f32 v19, v19, s12, v95
	v_cvt_pk_fp8_f32 v187, v22, v23
	v_pk_mul_f32 v[24:25], v[24:25], v[112:113] op_sel_hi:[1,0]
	v_pk_fma_f32 v[28:29], v[40:41], v[28:29], v[102:103]
	v_med3_f32 v32, v32, s12, v95
	v_med3_f32 v33, v33, s12, v95
	v_med3_f32 v14, v14, s12, v95
	v_med3_f32 v15, v15, s12, v95
	v_med3_f32 v10, v10, s12, v95
	v_med3_f32 v11, v11, s12, v95
	v_med3_f32 v6, v6, s12, v95
	v_med3_f32 v7, v7, s12, v95
	v_med3_f32 v2, v2, s12, v95
	v_med3_f32 v3, v3, s12, v95
	v_cvt_pk_fp8_f32 v188, v18, v19
	v_pk_mul_f32 v[20:21], v[20:21], v[112:113] op_sel_hi:[1,0]
	v_pk_fma_f32 v[24:25], v[44:45], v[24:25], v[106:107]
	v_med3_f32 v28, v28, s12, v95
	v_med3_f32 v29, v29, s12, v95
	v_cvt_pk_fp8_f32 v189, v14, v15
	v_cvt_pk_fp8_f32 v190, v10, v11
	v_cvt_pk_fp8_f32 v191, v6, v7
	v_cvt_pk_fp8_f32 v192, v2, v3
	v_cvt_pk_fp8_f32 v183, v32, v33 op_sel:[0,0,1]
	v_pk_mul_f32 v[16:17], v[16:17], v[112:113] op_sel_hi:[1,0]
	v_pk_mul_f32 v[12:13], v[12:13], v[112:113] op_sel_hi:[1,0]
	v_pk_mul_f32 v[8:9], v[8:9], v[112:113] op_sel_hi:[1,0]
	v_pk_mul_f32 v[4:5], v[4:5], v[112:113] op_sel_hi:[1,0]
	v_pk_fma_f32 v[20:21], v[48:49], v[20:21], v[110:111]
	v_med3_f32 v24, v24, s12, v95
	v_med3_f32 v25, v25, s12, v95
	v_cvt_pk_fp8_f32 v186, v28, v29 op_sel:[0,0,1]
	v_pk_fma_f32 v[16:17], v[52:53], v[16:17], v[146:147]
	v_pk_fma_f32 v[12:13], v[56:57], v[12:13], v[150:151]
	v_pk_fma_f32 v[8:9], v[60:61], v[8:9], v[154:155]
	v_pk_fma_f32 v[4:5], v[64:65], v[4:5], v[158:159]
	v_med3_f32 v20, v20, s12, v95
	v_med3_f32 v21, v21, s12, v95
	v_cvt_pk_fp8_f32 v187, v24, v25 op_sel:[0,0,1]
	v_med3_f32 v16, v16, s12, v95
	v_med3_f32 v17, v17, s12, v95
	v_med3_f32 v12, v12, s12, v95
	v_med3_f32 v13, v13, s12, v95
	v_med3_f32 v8, v8, s12, v95
	v_med3_f32 v9, v9, s12, v95
	v_med3_f32 v4, v4, s12, v95
	v_med3_f32 v5, v5, s12, v95
	v_cvt_pk_fp8_f32 v188, v20, v21 op_sel:[0,0,1]
	v_cvt_pk_fp8_f32 v189, v16, v17 op_sel:[0,0,1]
	v_cvt_pk_fp8_f32 v190, v12, v13 op_sel:[0,0,1]
	v_cvt_pk_fp8_f32 v191, v8, v9 op_sel:[0,0,1]
	v_cvt_pk_fp8_f32 v192, v4, v5 op_sel:[0,0,1]
	global_store_dword v[76:77], v183, off
	global_store_dword v[76:77], v186, off offset:256
	global_store_dword v[76:77], v187, off offset:512
	global_store_dword v[76:77], v188, off offset:768
	global_store_dword v[76:77], v189, off offset:1024
	global_store_dword v[76:77], v190, off offset:1280
	global_store_dword v[76:77], v191, off offset:1536
	global_store_dword v[76:77], v192, off offset:1792
	v_lshl_add_u64 v[76:77], v[76:77], 0, s[6:7]
	s_cbranch_scc1 .LBB0_1022

.LBB0_1024:
	s_andn2_b64 vcc, exec, s[6:7]
	s_cbranch_vccnz .LBB0_1026
	v_readlane_b32 s2, v249, 1
	v_readlane_b32 s3, v249, 2
	s_load_dwordx2 s[6:7], s[2:3], 0x20
	s_load_dwordx4 s[24:27], s[2:3], 0xd8
	s_ashr_i32 s1, s0, 31
	s_lshl_b64 s[10:11], s[0:1], 13
	s_add_u32 s20, s8, s10
	s_addc_u32 s21, s9, s11
	s_waitcnt lgkmcnt(0)
	s_add_u32 s3, s26, 0x100000
	s_addc_u32 s2, s27, 0
	s_lshr_b32 s12, s0, 11
	s_add_i32 s14, s0, 0x800
	s_mulk_i32 s12, 0x3000
	s_ashr_i32 s15, s14, 31
	s_ashr_i32 s13, s12, 31
	s_lshl_b64 s[18:19], s[14:15], 13
	s_lshl_b64 s[12:13], s[12:13], 2
	s_add_u32 s12, s3, s12
	s_addc_u32 s13, s2, s13
	s_add_u32 s16, s12, 0x2000
	v_lshlrev_b32_e32 v98, 4, v80
	s_addc_u32 s17, s13, 0
	global_load_dwordx4 v[66:69], v98, s[16:17]
	global_load_dwordx4 v[70:73], v98, s[6:7]
	v_or_b32_e32 v1, 0x400, v98
	v_or_b32_e32 v129, 0x800, v98
	global_load_dwordx4 v[74:77], v1, s[16:17]
	global_load_dwordx4 v[62:65], v98, s[20:21]
	global_load_dwordx4 v[46:49], v98, s[20:21] offset:1024
	global_load_dwordx4 v[82:85], v98, s[6:7] offset:1024
	global_load_dwordx4 v[30:33], v98, s[20:21] offset:2048
	global_load_dwordx4 v[14:17], v98, s[20:21] offset:3072
	global_load_dwordx4 v[90:93], v129, s[16:17]
	global_load_dwordx4 v[94:97], v98, s[6:7] offset:2048
	v_or_b32_e32 v130, 0xc00, v98
	global_load_dwordx4 v[118:121], v130, s[16:17]
	global_load_dwordx4 v[122:125], v98, s[6:7] offset:3072
	v_or_b32_e32 v126, 0x1000, v98
	global_load_dwordx4 v[140:143], v126, s[16:17]
	global_load_dwordx4 v[144:147], v126, s[6:7]
	v_mov_b32_e32 v99, 0
	v_lshl_add_u64 v[2:3], s[20:21], 0, v[98:99]
	v_add_co_u32_e32 v2, vcc, 0x1000, v2
	v_or_b32_e32 v127, 0x1400, v98
	v_mbcnt_lo_u32_b32 v4, -1, 0
	v_addc_co_u32_e32 v3, vcc, 0, v3, vcc
	global_load_dwordx4 v[86:89], v127, s[16:17]
	global_load_dwordx4 v[54:57], v[2:3], off nt
	global_load_dwordx4 v[38:41], v[2:3], off offset:1024 nt
	global_load_dwordx4 v[22:25], v[2:3], off offset:2048 nt
	global_load_dwordx4 v[6:9], v[2:3], off offset:3072 nt
	v_mbcnt_hi_u32_b32 v4, -1, v4
	v_and_b32_e32 v5, 64, v4
	v_add_u32_e32 v5, 64, v5
	v_xor_b32_e32 v10, 1, v4
	v_cmp_lt_i32_e32 vcc, v10, v5
	v_lshlrev_b32_e32 v2, 2, v80
	v_mov_b32_e32 v3, v99
	v_cndmask_b32_e32 v10, v4, v10, vcc
	v_lshlrev_b32_e32 v138, 2, v10
	v_xor_b32_e32 v10, 2, v4
	v_cmp_lt_i32_e32 vcc, v10, v5
	v_lshl_add_u64 v[102:103], s[8:9], 0, v[98:99]
	v_lshl_add_u64 v[2:3], s[26:27], 0, v[2:3]
	v_cndmask_b32_e32 v10, v4, v10, vcc
	v_lshlrev_b32_e32 v137, 2, v10
	v_xor_b32_e32 v10, 4, v4
	v_cmp_lt_i32_e32 vcc, v10, v5
	s_mov_b64 s[8:9], 0x42c00000
	v_lshl_add_u64 v[100:101], v[2:3], 0, s[8:9]
	v_cndmask_b32_e32 v10, v4, v10, vcc
	v_lshlrev_b32_e32 v136, 2, v10
	v_xor_b32_e32 v10, 8, v4
	v_cmp_lt_i32_e32 vcc, v10, v5
	v_lshl_add_u64 v[2:3], v[102:103], 0, s[18:19]
	global_load_dwordx4 v[58:61], v[2:3], off nt
	global_load_dwordx4 v[50:53], v[2:3], off offset:1024 nt
	global_load_dwordx4 v[42:45], v[2:3], off offset:2048 nt
	global_load_dwordx4 v[34:37], v[2:3], off offset:3072 nt
	v_cndmask_b32_e32 v10, v4, v10, vcc
	v_lshlrev_b32_e32 v135, 2, v10
	v_xor_b32_e32 v10, 16, v4
	v_cmp_lt_i32_e32 vcc, v10, v5
	s_movk_i32 s24, 0x1000
	v_or_b32_e32 v131, 0x1800, v98
	v_cndmask_b32_e32 v10, v4, v10, vcc
	v_lshlrev_b32_e32 v134, 2, v10
	v_xor_b32_e32 v10, 32, v4
	v_cmp_lt_i32_e32 vcc, v10, v5
	v_or_b32_e32 v128, 0x1c00, v98
	s_lshl_b64 s[8:9], s[0:1], 11
	v_cndmask_b32_e32 v4, v4, v10, vcc
	v_add_co_u32_e32 v2, vcc, s24, v2
	v_lshlrev_b32_e32 v133, 2, v4
	s_nop 0
	v_addc_co_u32_e32 v3, vcc, 0, v3, vcc
	global_load_dwordx4 v[26:29], v[2:3], off nt
	global_load_dwordx4 v[18:21], v[2:3], off offset:1024 nt
	global_load_dwordx4 v[10:13], v[2:3], off offset:2048 nt
	s_nop 0
	global_load_dwordx4 v[2:5], v[2:3], off offset:3072 nt
	s_lshr_b32 s1, s14, 11
	s_mov_b32 s20, 0x358637bd
	s_mov_b32 s23, 0x800000
	s_mov_b32 s22, 0xc3e00000
	s_waitcnt vmcnt(23)
	v_mov_b32_e32 v152, v63
	v_pk_add_f32 v[68:69], v[68:69], 1.0 op_sel_hi:[1,0]
	v_pk_add_f32 v[66:67], v[66:67], 1.0 op_sel_hi:[1,0]
	v_pk_mul_f32 v[114:115], v[72:73], v[68:69]
	v_pk_mul_f32 v[116:117], v[70:71], v[66:67]
	v_pk_add_f32 v[66:67], v[76:77], 1.0 op_sel_hi:[1,0]
	v_pk_add_f32 v[68:69], v[74:75], 1.0 op_sel_hi:[1,0]
	s_waitcnt vmcnt(21)
	v_pk_mul_f32 v[110:111], v[84:85], v[66:67]
	v_pk_mul_f32 v[112:113], v[82:83], v[68:69]
	s_waitcnt vmcnt(18)
	v_pk_add_f32 v[66:67], v[92:93], 1.0 op_sel_hi:[1,0]
	v_pk_add_f32 v[68:69], v[90:91], 1.0 op_sel_hi:[1,0]
	global_load_dwordx4 v[82:85], v98, s[12:13]
	global_load_dwordx4 v[78:81], v98, s[12:13] offset:1024
	s_waitcnt vmcnt(19)
	v_pk_mul_f32 v[106:107], v[96:97], v[66:67]
	v_pk_mul_f32 v[108:109], v[94:95], v[68:69]
	s_waitcnt vmcnt(18)
	v_pk_add_f32 v[66:67], v[120:121], 1.0 op_sel_hi:[1,0]
	v_pk_add_f32 v[68:69], v[118:119], 1.0 op_sel_hi:[1,0]
	global_load_dwordx4 v[74:77], v98, s[12:13] offset:2048
	global_load_dwordx4 v[70:73], v98, s[12:13] offset:3072
	global_load_dwordx4 v[118:121], v127, s[6:7]
	s_waitcnt vmcnt(19)
	v_pk_add_f32 v[90:91], v[142:143], 1.0 op_sel_hi:[1,0]
	v_pk_add_f32 v[92:93], v[140:141], 1.0 op_sel_hi:[1,0]
	v_pk_mul_f32 v[94:95], v[124:125], v[66:67]
	v_pk_mul_f32 v[96:97], v[122:123], v[68:69]
	global_load_dwordx4 v[66:69], v126, s[12:13]
	s_waitcnt vmcnt(19)
	v_pk_mul_f32 v[90:91], v[146:147], v[90:91]
	v_pk_mul_f32 v[92:93], v[144:145], v[92:93]
	global_load_dwordx4 v[122:125], v131, s[6:7]
	global_load_dwordx4 v[140:143], v131, s[16:17]
	global_load_dwordx4 v[144:147], v128, s[6:7]
	global_load_dwordx4 v[148:151], v128, s[16:17]
	v_mov_b32_e32 v153, v47
	v_mov_b32_e32 v104, v62
	v_mov_b32_e32 v105, v46
	v_pk_mul_f32 v[152:153], v[152:153], v[152:153]
	v_mov_b32_e32 v154, v65
	v_mov_b32_e32 v155, v49
	v_pk_fma_f32 v[104:105], v[104:105], v[104:105], v[152:153]
	v_mov_b32_e32 v152, v64
	v_mov_b32_e32 v153, v48
	v_pk_mul_f32 v[154:155], v[154:155], v[154:155]
	s_waitcnt vmcnt(21)
	v_mul_f32_e32 v132, v54, v54
	v_pk_fma_f32 v[152:153], v[152:153], v[152:153], v[154:155]
	v_pk_mul_f32 v[154:155], v[30:31], v[30:31]
	v_pk_add_f32 v[104:105], v[104:105], v[152:153]
	v_pk_mul_f32 v[152:153], v[32:33], v[32:33]
	v_mul_f32_e32 v139, v55, v55
	v_pk_mov_b32 v[156:157], v[154:155], v[152:153] op_sel:[1,0]
	v_mov_b32_e32 v155, v153
	v_pk_add_f32 v[152:153], v[156:157], v[154:155]
	v_pk_add_f32 v[104:105], v[104:105], v[104:105] op_sel:[0,1] op_sel_hi:[1,0]
	v_pk_add_f32 v[152:153], v[152:153], v[152:153] op_sel:[0,1] op_sel_hi:[1,0]
	v_mov_b32_e32 v105, v132
	v_mov_b32_e32 v153, v139
	v_mul_f32_e32 v132, v15, v15
	v_mul_f32_e32 v154, v56, v56
	v_pk_add_f32 v[104:105], v[104:105], v[152:153]
	v_pk_fma_f32 v[152:153], v[14:15], v[14:15], v[132:133] op_sel_hi:[1,1,0]
	v_mul_f32_e32 v132, v17, v17
	v_mul_f32_e32 v156, v57, v57
	v_mov_b32_e32 v153, v154
	v_pk_fma_f32 v[154:155], v[16:17], v[16:17], v[132:133] op_sel_hi:[1,1,0]
	s_waitcnt vmcnt(18)
	v_mul_f32_e32 v132, v6, v6
	v_mov_b32_e32 v155, v156
	v_pk_add_f32 v[152:153], v[152:153], v[154:155]
	v_pk_mul_f32 v[154:155], v[38:39], v[38:39]
	v_pk_add_f32 v[104:105], v[104:105], v[152:153]
	v_pk_mul_f32 v[152:153], v[40:41], v[40:41]
	v_mul_f32_e32 v139, v7, v7
	v_pk_mov_b32 v[156:157], v[154:155], v[152:153] op_sel:[1,0]
	v_mov_b32_e32 v155, v153
	v_pk_add_f32 v[152:153], v[156:157], v[154:155]
	v_pk_add_f32 v[104:105], v[104:105], v[104:105] op_sel:[0,1] op_sel_hi:[1,0]
	v_pk_add_f32 v[152:153], v[152:153], v[152:153] op_sel:[0,1] op_sel_hi:[1,0]
	v_mov_b32_e32 v105, v132
	v_mov_b32_e32 v153, v139
	v_mul_f32_e32 v132, v23, v23
	v_mul_f32_e32 v154, v8, v8
	v_pk_add_f32 v[104:105], v[104:105], v[152:153]
	v_pk_fma_f32 v[152:153], v[22:23], v[22:23], v[132:133] op_sel_hi:[1,1,0]
	v_mul_f32_e32 v132, v25, v25
	v_mul_f32_e32 v156, v9, v9
	v_mov_b32_e32 v153, v154
	v_pk_fma_f32 v[154:155], v[24:25], v[24:25], v[132:133] op_sel_hi:[1,1,0]
	s_waitcnt vmcnt(16)
	v_mov_b32_e32 v157, v53
	v_mov_b32_e32 v155, v156
	v_pk_add_f32 v[152:153], v[152:153], v[154:155]
	v_mov_b32_e32 v154, v59
	v_mov_b32_e32 v155, v51
	v_pk_add_f32 v[104:105], v[104:105], v[152:153]
	v_mov_b32_e32 v152, v58
	v_mov_b32_e32 v153, v50
	v_pk_mul_f32 v[154:155], v[154:155], v[154:155]
	v_mov_b32_e32 v156, v61
	v_pk_fma_f32 v[152:153], v[152:153], v[152:153], v[154:155]
	v_mov_b32_e32 v154, v60
	v_mov_b32_e32 v155, v52
	v_pk_mul_f32 v[156:157], v[156:157], v[156:157]
	s_waitcnt vmcnt(13)
	v_mul_f32_e32 v132, v26, v26
	v_pk_fma_f32 v[154:155], v[154:155], v[154:155], v[156:157]
	v_pk_mul_f32 v[156:157], v[42:43], v[42:43]
	v_pk_add_f32 v[152:153], v[152:153], v[154:155]
	v_pk_mul_f32 v[154:155], v[44:45], v[44:45]
	v_mul_f32_e32 v139, v27, v27
	v_pk_mov_b32 v[158:159], v[156:157], v[154:155] op_sel:[1,0]
	v_mov_b32_e32 v157, v155
	v_pk_add_f32 v[154:155], v[158:159], v[156:157]
	v_pk_add_f32 v[152:153], v[152:153], v[152:153] op_sel:[0,1] op_sel_hi:[1,0]
	v_pk_add_f32 v[154:155], v[154:155], v[154:155] op_sel:[0,1] op_sel_hi:[1,0]
	v_mov_b32_e32 v153, v132
	v_mov_b32_e32 v155, v139
	v_mul_f32_e32 v132, v35, v35
	v_mul_f32_e32 v156, v28, v28
	v_pk_add_f32 v[152:153], v[152:153], v[154:155]
	v_pk_fma_f32 v[154:155], v[34:35], v[34:35], v[132:133] op_sel_hi:[1,1,0]
	v_mul_f32_e32 v132, v37, v37
	v_mul_f32_e32 v158, v29, v29
	v_mov_b32_e32 v155, v156
	v_pk_fma_f32 v[156:157], v[36:37], v[36:37], v[132:133] op_sel_hi:[1,1,0]
	s_waitcnt vmcnt(10)
	v_mul_f32_e32 v132, v2, v2
	v_mov_b32_e32 v157, v158
	v_pk_add_f32 v[154:155], v[154:155], v[156:157]
	v_pk_mul_f32 v[156:157], v[18:19], v[18:19]
	v_pk_add_f32 v[152:153], v[152:153], v[154:155]
	v_pk_mul_f32 v[154:155], v[20:21], v[20:21]
	v_mul_f32_e32 v139, v3, v3
	v_pk_mov_b32 v[158:159], v[156:157], v[154:155] op_sel:[1,0]
	v_mov_b32_e32 v157, v155
	v_pk_add_f32 v[154:155], v[158:159], v[156:157]
	v_pk_add_f32 v[152:153], v[152:153], v[152:153] op_sel:[0,1] op_sel_hi:[1,0]
	v_pk_add_f32 v[154:155], v[154:155], v[154:155] op_sel:[0,1] op_sel_hi:[1,0]
	v_mov_b32_e32 v153, v132
	v_mov_b32_e32 v155, v139
	v_mul_f32_e32 v132, v11, v11
	v_mul_f32_e32 v156, v4, v4
	v_pk_add_f32 v[152:153], v[152:153], v[154:155]
	v_pk_fma_f32 v[154:155], v[10:11], v[10:11], v[132:133] op_sel_hi:[1,1,0]
	v_mul_f32_e32 v132, v13, v13
	v_mul_f32_e32 v158, v5, v5
	v_mov_b32_e32 v155, v156
	v_pk_fma_f32 v[156:157], v[12:13], v[12:13], v[132:133] op_sel_hi:[1,1,0]
	v_pk_add_f32 v[88:89], v[88:89], 1.0 op_sel_hi:[1,0]
	v_mov_b32_e32 v157, v158
	v_pk_add_f32 v[154:155], v[154:155], v[156:157]
	v_pk_add_f32 v[86:87], v[86:87], 1.0 op_sel_hi:[1,0]
	v_pk_add_f32 v[152:153], v[152:153], v[154:155]
	v_mov_b32_e32 v155, v104
	v_mov_b32_e32 v154, v152
	v_mov_b32_e32 v104, v153
	v_pk_add_f32 v[104:105], v[154:155], v[104:105]
	global_load_dwordx4 v[152:155], v127, s[12:13]
	ds_bpermute_b32 v157, v138, v105
	ds_bpermute_b32 v156, v138, v104
	s_waitcnt vmcnt(6)
	v_pk_mul_f32 v[88:89], v[120:121], v[88:89]
	v_pk_mul_f32 v[158:159], v[118:119], v[86:87]
	global_load_dwordx4 v[118:121], v131, s[12:13]
	s_waitcnt vmcnt(4)
	v_pk_add_f32 v[142:143], v[142:143], 1.0 op_sel_hi:[1,0]
	s_waitcnt lgkmcnt(0)
	v_pk_add_f32 v[86:87], v[104:105], v[156:157]
	ds_bpermute_b32 v105, v137, v87
	ds_bpermute_b32 v104, v137, v86
	v_pk_add_f32 v[140:141], v[140:141], 1.0 op_sel_hi:[1,0]
	v_pk_mul_f32 v[142:143], v[124:125], v[142:143]
	v_pk_mul_f32 v[140:141], v[122:123], v[140:141]
	global_load_dwordx4 v[122:125], v128, s[12:13]
	s_waitcnt lgkmcnt(0)
	v_pk_add_f32 v[86:87], v[86:87], v[104:105]
	ds_bpermute_b32 v105, v136, v87
	ds_bpermute_b32 v104, v136, v86
	s_waitcnt vmcnt(3)
	v_pk_add_f32 v[148:149], v[148:149], 1.0 op_sel_hi:[1,0]
	s_add_i32 s12, s0, 0x1000
	v_pk_mul_f32 v[144:145], v[144:145], v[148:149]
	v_lshl_add_u64 v[148:149], v[100:101], 0, s[8:9]
	s_waitcnt lgkmcnt(0)
	v_pk_add_f32 v[86:87], v[86:87], v[104:105]
	ds_bpermute_b32 v105, v135, v87
	ds_bpermute_b32 v104, v135, v86
	s_mul_i32 s8, s1, 0x3000
	s_ashr_i32 s13, s12, 31
	s_ashr_i32 s9, s8, 31
	s_lshl_b64 s[18:19], s[12:13], 13
	s_waitcnt lgkmcnt(0)
	v_pk_add_f32 v[86:87], v[86:87], v[104:105]
	ds_bpermute_b32 v105, v134, v87
	ds_bpermute_b32 v104, v134, v86
	s_lshl_b64 s[8:9], s[8:9], 2
	s_add_u32 s16, s3, s8
	s_mov_b32 s8, 0x3a000000
	v_pk_add_f32 v[150:151], v[150:151], 1.0 op_sel_hi:[1,0]
	s_waitcnt lgkmcnt(0)
	v_pk_add_f32 v[86:87], v[86:87], v[104:105]
	ds_bpermute_b32 v105, v133, v87
	ds_bpermute_b32 v104, v133, v86
	v_pk_mul_f32 v[146:147], v[146:147], v[150:151]
	s_addc_u32 s17, s2, s9
	s_waitcnt lgkmcnt(0)
	v_pk_add_f32 v[86:87], v[86:87], v[104:105]
	v_mov_b64_e32 v[104:105], s[20:21]
	v_pk_fma_f32 v[86:87], v[86:87], s[8:9], v[104:105] op_sel_hi:[1,0,0]
	s_add_u32 s20, s16, 0x2000
	v_mul_f32_e32 v132, 0x4b800000, v87
	v_cmp_gt_f32_e32 vcc, s23, v87
	s_addc_u32 s21, s17, 0
	s_lshl_b64 s[14:15], s[14:15], 11
	v_cndmask_b32_e32 v87, v87, v132, vcc
	v_rsq_f32_e32 v87, v87
	s_lshr_b32 s1, s12, 11
	v_mul_f32_e32 v132, 0x45800000, v87
	v_cndmask_b32_e32 v150, v87, v132, vcc
	v_pk_mul_f32 v[62:63], v[62:63], v[150:151] op_sel_hi:[1,0]
	v_mov_b32_e32 v132, 0x43e00000
	v_pk_fma_f32 v[62:63], v[116:117], v[62:63], v[82:83]
	v_mov_b32_e32 v82, v99
	v_med3_f32 v62, v62, s22, v132
	v_med3_f32 v63, v63, s22, v132
	v_cvt_pk_fp8_f32 v82, v62, v63
	v_pk_mul_f32 v[64:65], v[64:65], v[150:151] op_sel_hi:[1,0]
	v_pk_mul_f32 v[46:47], v[46:47], v[150:151] op_sel_hi:[1,0]
	v_pk_fma_f32 v[62:63], v[114:115], v[64:65], v[84:85]
	v_pk_fma_f32 v[46:47], v[112:113], v[46:47], v[78:79]
	v_med3_f32 v62, v62, s22, v132
	v_med3_f32 v63, v63, s22, v132
	v_cvt_pk_fp8_f32 v82, v62, v63 op_sel:[0,0,1]
	v_med3_f32 v46, v46, s22, v132
	v_med3_f32 v47, v47, s22, v132
	v_mov_b32_e32 v62, v99
	v_cvt_pk_fp8_f32 v62, v46, v47
	v_pk_mul_f32 v[48:49], v[48:49], v[150:151] op_sel_hi:[1,0]
	v_pk_mul_f32 v[30:31], v[30:31], v[150:151] op_sel_hi:[1,0]
	v_pk_fma_f32 v[46:47], v[110:111], v[48:49], v[80:81]
	v_pk_fma_f32 v[30:31], v[108:109], v[30:31], v[74:75]
	v_med3_f32 v46, v46, s22, v132
	v_med3_f32 v47, v47, s22, v132
	v_cvt_pk_fp8_f32 v62, v46, v47 op_sel:[0,0,1]
	v_med3_f32 v30, v30, s22, v132
	v_med3_f32 v31, v31, s22, v132
	v_mov_b32_e32 v46, v99
	v_cvt_pk_fp8_f32 v46, v30, v31
	v_pk_mul_f32 v[32:33], v[32:33], v[150:151] op_sel_hi:[1,0]
	v_pk_mul_f32 v[14:15], v[14:15], v[150:151] op_sel_hi:[1,0]
	v_pk_fma_f32 v[30:31], v[106:107], v[32:33], v[76:77]
	v_pk_fma_f32 v[14:15], v[96:97], v[14:15], v[70:71]
	v_med3_f32 v30, v30, s22, v132
	v_med3_f32 v31, v31, s22, v132
	v_cvt_pk_fp8_f32 v46, v30, v31 op_sel:[0,0,1]
	v_med3_f32 v14, v14, s22, v132
	v_med3_f32 v15, v15, s22, v132
	v_mov_b32_e32 v30, v99
	v_cvt_pk_fp8_f32 v30, v14, v15
	v_pk_mul_f32 v[16:17], v[16:17], v[150:151] op_sel_hi:[1,0]
	v_mov_b32_e32 v31, v99
	v_pk_fma_f32 v[14:15], v[94:95], v[16:17], v[72:73]
	v_pk_mul_f32 v[16:17], v[56:57], v[150:151] op_sel_hi:[1,0]
	v_med3_f32 v14, v14, s22, v132
	v_med3_f32 v15, v15, s22, v132
	v_cvt_pk_fp8_f32 v30, v14, v15 op_sel:[0,0,1]
	v_pk_mul_f32 v[14:15], v[54:55], v[150:151] op_sel_hi:[1,0]
	global_store_dword v[148:149], v82, off
	global_store_dword v[148:149], v62, off offset:256
	global_store_dword v[148:149], v46, off offset:512
	global_store_dword v[148:149], v30, off offset:768
	v_pk_fma_f32 v[14:15], v[92:93], v[14:15], v[66:67]
	v_mov_b32_e32 v30, v99
	v_med3_f32 v14, v14, s22, v132
	v_med3_f32 v15, v15, s22, v132
	v_cvt_pk_fp8_f32 v30, v14, v15
	v_pk_fma_f32 v[14:15], v[90:91], v[16:17], v[68:69]
	v_pk_mul_f32 v[16:17], v[40:41], v[150:151] op_sel_hi:[1,0]
	v_med3_f32 v14, v14, s22, v132
	v_med3_f32 v15, v15, s22, v132
	v_cvt_pk_fp8_f32 v30, v14, v15 op_sel:[0,0,1]
	v_pk_mul_f32 v[14:15], v[38:39], v[150:151] op_sel_hi:[1,0]
	v_pk_mul_f32 v[6:7], v[6:7], v[150:151] op_sel_hi:[1,0]
	s_waitcnt vmcnt(6)
	v_pk_fma_f32 v[14:15], v[158:159], v[14:15], v[152:153]
	s_waitcnt vmcnt(4)
	v_pk_fma_f32 v[6:7], v[144:145], v[6:7], v[122:123]
	v_med3_f32 v14, v14, s22, v132
	v_med3_f32 v15, v15, s22, v132
	v_cvt_pk_fp8_f32 v31, v14, v15
	v_pk_fma_f32 v[14:15], v[88:89], v[16:17], v[154:155]
	v_pk_mul_f32 v[16:17], v[24:25], v[150:151] op_sel_hi:[1,0]
	v_med3_f32 v14, v14, s22, v132
	v_med3_f32 v15, v15, s22, v132
	v_cvt_pk_fp8_f32 v31, v14, v15 op_sel:[0,0,1]
	v_pk_mul_f32 v[14:15], v[22:23], v[150:151] op_sel_hi:[1,0]
	v_mov_b32_e32 v22, v99
	v_pk_fma_f32 v[14:15], v[140:141], v[14:15], v[118:119]
	v_med3_f32 v6, v6, s22, v132
	v_med3_f32 v14, v14, s22, v132
	v_med3_f32 v15, v15, s22, v132
	v_cvt_pk_fp8_f32 v22, v14, v15
	v_pk_fma_f32 v[14:15], v[142:143], v[16:17], v[120:121]
	v_med3_f32 v7, v7, s22, v132
	v_med3_f32 v14, v14, s22, v132
	v_med3_f32 v15, v15, s22, v132
	v_cvt_pk_fp8_f32 v22, v14, v15 op_sel:[0,0,1]
	v_mov_b32_e32 v14, v99
	v_cvt_pk_fp8_f32 v14, v6, v7
	v_pk_mul_f32 v[8:9], v[8:9], v[150:151] op_sel_hi:[1,0]
	s_nop 0
	v_pk_fma_f32 v[6:7], v[146:147], v[8:9], v[124:125]
	s_nop 0
	v_med3_f32 v6, v6, s22, v132
	v_med3_f32 v7, v7, s22, v132
	v_cvt_pk_fp8_f32 v14, v6, v7 op_sel:[0,0,1]
	global_store_dword v[148:149], v30, off offset:1024
	global_store_dword v[148:149], v31, off offset:1280
	global_store_dword v[148:149], v22, off offset:1536
	global_store_dword v[148:149], v14, off offset:1792
	global_load_dwordx4 v[66:69], v98, s[20:21]
	global_load_dwordx4 v[70:73], v98, s[6:7]
	global_load_dwordx4 v[74:77], v1, s[20:21]
	global_load_dwordx4 v[78:81], v98, s[6:7] offset:1024
	global_load_dwordx4 v[82:85], v129, s[20:21]
	global_load_dwordx4 v[88:91], v98, s[6:7] offset:2048
	global_load_dwordx4 v[92:95], v130, s[20:21]
	global_load_dwordx4 v[106:109], v98, s[6:7] offset:3072
	global_load_dwordx4 v[110:113], v126, s[20:21]
	global_load_dwordx4 v[114:117], v126, s[6:7]
	global_load_dwordx4 v[118:121], v127, s[20:21]
	global_load_dwordx4 v[122:125], v127, s[6:7]
	global_load_dwordx4 v[140:143], v131, s[20:21]
	global_load_dwordx4 v[144:147], v131, s[6:7]
	global_load_dwordx4 v[148:151], v128, s[20:21]
	global_load_dwordx4 v[152:155], v128, s[6:7]
	global_load_dwordx4 v[156:159], v98, s[16:17]
	global_load_dwordx4 v[160:163], v98, s[16:17] offset:1024
	v_lshl_add_u64 v[6:7], v[102:103], 0, s[18:19]
	global_load_dwordx4 v[62:65], v[6:7], off nt
	global_load_dwordx4 v[54:57], v[6:7], off offset:1024 nt
	global_load_dwordx4 v[164:167], v98, s[16:17] offset:2048
	global_load_dwordx4 v[46:49], v[6:7], off offset:2048 nt
	global_load_dwordx4 v[38:41], v[6:7], off offset:3072 nt
	v_add_co_u32_e32 v6, vcc, s24, v6
	s_waitcnt vmcnt(22)
	v_pk_add_f32 v[68:69], v[68:69], 1.0 op_sel_hi:[1,0]
	v_addc_co_u32_e32 v7, vcc, 0, v7, vcc
	global_load_dwordx4 v[30:33], v[6:7], off nt
	global_load_dwordx4 v[22:25], v[6:7], off offset:1024 nt
	global_load_dwordx4 v[14:17], v[6:7], off offset:2048 nt
	s_nop 0
	global_load_dwordx4 v[6:9], v[6:7], off offset:3072 nt
	s_nop 0
	global_load_dwordx4 v[168:171], v98, s[16:17] offset:3072
	v_pk_add_f32 v[66:67], v[66:67], 1.0 op_sel_hi:[1,0]
	s_waitcnt vmcnt(26)
	v_pk_mul_f32 v[96:97], v[72:73], v[68:69]
	v_pk_mul_f32 v[172:173], v[70:71], v[66:67]
	s_waitcnt vmcnt(25)
	v_pk_add_f32 v[66:67], v[76:77], 1.0 op_sel_hi:[1,0]
	v_pk_add_f32 v[68:69], v[74:75], 1.0 op_sel_hi:[1,0]
	s_waitcnt vmcnt(24)
	v_pk_mul_f32 v[174:175], v[80:81], v[66:67]
	v_pk_mul_f32 v[176:177], v[78:79], v[68:69]
	s_waitcnt vmcnt(23)
	v_pk_add_f32 v[66:67], v[84:85], 1.0 op_sel_hi:[1,0]
	v_pk_add_f32 v[68:69], v[82:83], 1.0 op_sel_hi:[1,0]
	s_waitcnt vmcnt(22)
	v_pk_mul_f32 v[82:83], v[90:91], v[66:67]
	v_pk_mul_f32 v[84:85], v[88:89], v[68:69]
	global_load_dwordx4 v[66:69], v126, s[16:17]
	s_waitcnt vmcnt(22)
	v_pk_add_f32 v[70:71], v[94:95], 1.0 op_sel_hi:[1,0]
	v_pk_add_f32 v[72:73], v[92:93], 1.0 op_sel_hi:[1,0]
	s_waitcnt vmcnt(21)
	v_pk_mul_f32 v[88:89], v[108:109], v[70:71]
	v_pk_mul_f32 v[90:91], v[106:107], v[72:73]
	s_waitcnt vmcnt(20)
	v_pk_add_f32 v[70:71], v[112:113], 1.0 op_sel_hi:[1,0]
	v_pk_add_f32 v[72:73], v[110:111], 1.0 op_sel_hi:[1,0]
	s_waitcnt vmcnt(19)
	v_pk_mul_f32 v[92:93], v[116:117], v[70:71]
	v_pk_mul_f32 v[94:95], v[114:115], v[72:73]
	global_load_dwordx4 v[70:73], v127, s[16:17]
	s_waitcnt vmcnt(19)
	v_pk_add_f32 v[74:75], v[120:121], 1.0 op_sel_hi:[1,0]
	v_pk_add_f32 v[76:77], v[118:119], 1.0 op_sel_hi:[1,0]
	s_waitcnt vmcnt(18)
	v_pk_mul_f32 v[106:107], v[124:125], v[74:75]
	v_pk_mul_f32 v[108:109], v[122:123], v[76:77]
	global_load_dwordx4 v[74:77], v131, s[16:17]
	s_waitcnt vmcnt(18)
	v_pk_add_f32 v[78:79], v[142:143], 1.0 op_sel_hi:[1,0]
	v_cmp_gt_f32_e32 vcc, s23, v86
	s_waitcnt vmcnt(17)
	v_pk_mul_f32 v[110:111], v[146:147], v[78:79]
	v_mul_f32_e32 v78, 0x4b800000, v86
	v_pk_add_f32 v[80:81], v[140:141], 1.0 op_sel_hi:[1,0]
	v_cndmask_b32_e32 v78, v86, v78, vcc
	v_pk_mul_f32 v[112:113], v[144:145], v[80:81]
	v_rsq_f32_e32 v118, v78
	global_load_dwordx4 v[78:81], v128, s[16:17]
	s_waitcnt vmcnt(17)
	v_pk_add_f32 v[114:115], v[150:151], 1.0 op_sel_hi:[1,0]
	v_pk_add_f32 v[116:117], v[148:149], 1.0 op_sel_hi:[1,0]
	s_waitcnt vmcnt(16)
	v_pk_mul_f32 v[86:87], v[154:155], v[114:115]
	v_pk_mul_f32 v[114:115], v[152:153], v[116:117]
	v_mul_f32_e32 v116, 0x45800000, v118
	v_cndmask_b32_e32 v116, v118, v116, vcc
	v_pk_mul_f32 v[58:59], v[58:59], v[116:117] op_sel_hi:[1,0]
	v_pk_mul_f32 v[60:61], v[60:61], v[116:117] op_sel_hi:[1,0]
	s_waitcnt vmcnt(15)
	v_pk_fma_f32 v[58:59], v[172:173], v[58:59], v[156:157]
	v_mov_b32_e32 v117, v99
	v_med3_f32 v58, v58, s22, v132
	v_med3_f32 v59, v59, s22, v132
	v_cvt_pk_fp8_f32 v117, v58, v59
	v_pk_fma_f32 v[58:59], v[96:97], v[60:61], v[158:159]
	v_lshl_add_u64 v[118:119], v[100:101], 0, s[14:15]
	v_med3_f32 v58, v58, s22, v132
	v_med3_f32 v59, v59, s22, v132
	v_cvt_pk_fp8_f32 v117, v58, v59 op_sel:[0,0,1]
	v_mov_b32_e32 v58, v99
	s_mul_i32 s14, s1, 0x3000
	s_ashr_i32 s15, s14, 31
	v_pk_mul_f32 v[50:51], v[50:51], v[116:117] op_sel_hi:[1,0]
	v_pk_mul_f32 v[52:53], v[52:53], v[116:117] op_sel_hi:[1,0]
	s_waitcnt vmcnt(14)
	v_pk_fma_f32 v[50:51], v[176:177], v[50:51], v[160:161]
	v_pk_mul_f32 v[42:43], v[42:43], v[116:117] op_sel_hi:[1,0]
	v_med3_f32 v50, v50, s22, v132
	v_med3_f32 v51, v51, s22, v132
	v_cvt_pk_fp8_f32 v58, v50, v51
	v_pk_fma_f32 v[50:51], v[174:175], v[52:53], v[162:163]
	s_waitcnt vmcnt(11)
	v_pk_fma_f32 v[42:43], v[84:85], v[42:43], v[164:165]
	v_med3_f32 v50, v50, s22, v132
	v_med3_f32 v51, v51, s22, v132
	v_cvt_pk_fp8_f32 v58, v50, v51 op_sel:[0,0,1]
	v_med3_f32 v42, v42, s22, v132
	v_med3_f32 v43, v43, s22, v132
	v_mov_b32_e32 v50, v99
	v_cvt_pk_fp8_f32 v50, v42, v43
	v_pk_mul_f32 v[44:45], v[44:45], v[116:117] op_sel_hi:[1,0]
	v_pk_mul_f32 v[34:35], v[34:35], v[116:117] op_sel_hi:[1,0]
	v_pk_fma_f32 v[42:43], v[82:83], v[44:45], v[166:167]
	v_pk_mul_f32 v[36:37], v[36:37], v[116:117] op_sel_hi:[1,0]
	v_med3_f32 v42, v42, s22, v132
	v_med3_f32 v43, v43, s22, v132
	v_cvt_pk_fp8_f32 v50, v42, v43 op_sel:[0,0,1]
	s_waitcnt vmcnt(4)
	v_pk_fma_f32 v[34:35], v[90:91], v[34:35], v[168:169]
	v_mov_b32_e32 v42, v99
	v_med3_f32 v34, v34, s22, v132
	v_med3_f32 v35, v35, s22, v132
	v_cvt_pk_fp8_f32 v42, v34, v35
	v_pk_fma_f32 v[34:35], v[88:89], v[36:37], v[170:171]
	v_pk_mul_f32 v[26:27], v[26:27], v[116:117] op_sel_hi:[1,0]
	v_med3_f32 v34, v34, s22, v132
	v_med3_f32 v35, v35, s22, v132
	v_cvt_pk_fp8_f32 v42, v34, v35 op_sel:[0,0,1]
	v_mov_b32_e32 v34, v99
	v_pk_mul_f32 v[28:29], v[28:29], v[116:117] op_sel_hi:[1,0]
	s_waitcnt vmcnt(3)
	v_pk_fma_f32 v[26:27], v[94:95], v[26:27], v[66:67]
	v_pk_mul_f32 v[18:19], v[18:19], v[116:117] op_sel_hi:[1,0]
	v_med3_f32 v26, v26, s22, v132
	v_med3_f32 v27, v27, s22, v132
	v_cvt_pk_fp8_f32 v34, v26, v27
	v_pk_fma_f32 v[26:27], v[92:93], v[28:29], v[68:69]
	v_pk_mul_f32 v[20:21], v[20:21], v[116:117] op_sel_hi:[1,0]
	v_med3_f32 v26, v26, s22, v132
	v_med3_f32 v27, v27, s22, v132
	s_waitcnt vmcnt(2)
	v_pk_fma_f32 v[18:19], v[108:109], v[18:19], v[70:71]
	v_cvt_pk_fp8_f32 v34, v26, v27 op_sel:[0,0,1]
	v_med3_f32 v18, v18, s22, v132
	v_med3_f32 v19, v19, s22, v132
	v_mov_b32_e32 v26, v99
	v_cvt_pk_fp8_f32 v26, v18, v19
	v_pk_fma_f32 v[18:19], v[106:107], v[20:21], v[72:73]
	v_pk_mul_f32 v[10:11], v[10:11], v[116:117] op_sel_hi:[1,0]
	v_med3_f32 v18, v18, s22, v132
	v_med3_f32 v19, v19, s22, v132
	s_waitcnt vmcnt(1)
	v_pk_fma_f32 v[10:11], v[112:113], v[10:11], v[74:75]
	v_cvt_pk_fp8_f32 v26, v18, v19 op_sel:[0,0,1]
	v_med3_f32 v10, v10, s22, v132
	v_med3_f32 v11, v11, s22, v132
	v_mov_b32_e32 v18, v99
	v_cvt_pk_fp8_f32 v18, v10, v11
	v_pk_mul_f32 v[12:13], v[12:13], v[116:117] op_sel_hi:[1,0]
	v_pk_mul_f32 v[2:3], v[2:3], v[116:117] op_sel_hi:[1,0]
	v_pk_fma_f32 v[10:11], v[110:111], v[12:13], v[76:77]
	s_waitcnt vmcnt(0)
	v_pk_fma_f32 v[2:3], v[114:115], v[2:3], v[78:79]
	v_med3_f32 v10, v10, s22, v132
	v_med3_f32 v11, v11, s22, v132
	v_cvt_pk_fp8_f32 v18, v10, v11 op_sel:[0,0,1]
	v_med3_f32 v2, v2, s22, v132
	v_med3_f32 v3, v3, s22, v132
	v_mov_b32_e32 v10, v99
	v_cvt_pk_fp8_f32 v10, v2, v3
	v_pk_mul_f32 v[4:5], v[4:5], v[116:117] op_sel_hi:[1,0]
	s_lshl_b64 s[14:15], s[14:15], 2
	v_pk_fma_f32 v[2:3], v[86:87], v[4:5], v[80:81]
	s_add_u32 s14, s3, s14
	v_med3_f32 v2, v2, s22, v132
	v_med3_f32 v3, v3, s22, v132
	s_addc_u32 s15, s2, s15
	v_cvt_pk_fp8_f32 v10, v2, v3 op_sel:[0,0,1]
	s_add_u32 s16, s14, 0x2000
	global_store_dword v[118:119], v117, off
	global_store_dword v[118:119], v58, off offset:256
	global_store_dword v[118:119], v50, off offset:512
	global_store_dword v[118:119], v42, off offset:768
	global_store_dword v[118:119], v34, off offset:1024
	global_store_dword v[118:119], v26, off offset:1280
	global_store_dword v[118:119], v18, off offset:1536
	global_store_dword v[118:119], v10, off offset:1792
	s_addc_u32 s17, s15, 0
	global_load_dwordx4 v[66:69], v98, s[16:17]
	global_load_dwordx4 v[70:73], v98, s[6:7]
	global_load_dwordx4 v[74:77], v1, s[16:17]
	global_load_dwordx4 v[78:81], v98, s[6:7] offset:1024
	global_load_dwordx4 v[90:93], v129, s[16:17]
	global_load_dwordx4 v[120:123], v98, s[6:7] offset:2048
	global_load_dwordx4 v[140:143], v130, s[16:17]
	global_load_dwordx4 v[144:147], v98, s[6:7] offset:3072
	global_load_dwordx4 v[148:151], v126, s[16:17]
	global_load_dwordx4 v[152:155], v126, s[6:7]
	global_load_dwordx4 v[156:159], v127, s[16:17]
	v_lshl_add_u64 v[94:95], v[102:103], 0, s[10:11]
	s_mov_b32 s1, 0x3001000
	s_mov_b64 s[10:11], 0x3000000
	v_add_co_u32_e32 v4, vcc, s1, v94
	v_lshl_add_u64 v[2:3], v[94:95], 0, s[10:11]
	s_nop 0
	v_addc_co_u32_e32 v5, vcc, 0, v95, vcc
	global_load_dwordx4 v[50:53], v[2:3], off offset:1024 nt
	global_load_dwordx4 v[42:45], v[2:3], off offset:2048 nt
	global_load_dwordx4 v[34:37], v[2:3], off offset:3072 nt
	global_load_dwordx4 v[58:61], v[4:5], off offset:-4096
	global_load_dwordx4 v[26:29], v[4:5], off nt
	global_load_dwordx4 v[18:21], v[4:5], off offset:1024 nt
	global_load_dwordx4 v[10:13], v[4:5], off offset:2048 nt
	s_nop 0
	global_load_dwordx4 v[2:5], v[4:5], off offset:3072 nt
	v_mul_f32_e32 v139, v30, v30
	global_load_dwordx4 v[86:89], v128, s[16:17]
	s_lshl_b64 s[10:11], s[12:13], 11
	s_mul_i32 s1, s81, 24
	s_waitcnt vmcnt(19)
	v_pk_add_f32 v[68:69], v[68:69], 1.0 op_sel_hi:[1,0]
	v_pk_add_f32 v[66:67], v[66:67], 1.0 op_sel_hi:[1,0]
	s_waitcnt vmcnt(18)
	v_pk_mul_f32 v[108:109], v[72:73], v[68:69]
	v_pk_mul_f32 v[112:113], v[70:71], v[66:67]
	s_waitcnt vmcnt(17)
	v_pk_add_f32 v[66:67], v[76:77], 1.0 op_sel_hi:[1,0]
	v_pk_add_f32 v[68:69], v[74:75], 1.0 op_sel_hi:[1,0]
	s_waitcnt vmcnt(16)
	v_pk_mul_f32 v[116:117], v[80:81], v[66:67]
	v_pk_mul_f32 v[118:119], v[78:79], v[68:69]
	s_waitcnt vmcnt(15)
	v_pk_add_f32 v[66:67], v[92:93], 1.0 op_sel_hi:[1,0]
	v_pk_add_f32 v[68:69], v[90:91], 1.0 op_sel_hi:[1,0]
	global_load_dwordx4 v[82:85], v98, s[14:15]
	global_load_dwordx4 v[78:81], v98, s[14:15] offset:1024
	s_waitcnt vmcnt(16)
	v_pk_mul_f32 v[110:111], v[122:123], v[66:67]
	v_pk_mul_f32 v[114:115], v[120:121], v[68:69]
	global_load_dwordx4 v[74:77], v98, s[14:15] offset:2048
	global_load_dwordx4 v[70:73], v98, s[14:15] offset:3072
	global_load_dwordx4 v[120:123], v127, s[6:7]
	s_waitcnt vmcnt(18)
	v_pk_add_f32 v[66:67], v[142:143], 1.0 op_sel_hi:[1,0]
	v_pk_add_f32 v[68:69], v[140:141], 1.0 op_sel_hi:[1,0]
	s_waitcnt vmcnt(17)
	v_pk_mul_f32 v[96:97], v[146:147], v[66:67]
	v_pk_mul_f32 v[106:107], v[144:145], v[68:69]
	s_waitcnt vmcnt(16)
	v_pk_add_f32 v[90:91], v[150:151], 1.0 op_sel_hi:[1,0]
	v_pk_add_f32 v[92:93], v[148:149], 1.0 op_sel_hi:[1,0]
	global_load_dwordx4 v[66:69], v126, s[14:15]
	global_load_dwordx4 v[140:143], v131, s[6:7]
	global_load_dwordx4 v[144:147], v131, s[16:17]
	global_load_dwordx4 v[148:151], v128, s[6:7]
	s_waitcnt vmcnt(19)
	v_pk_mul_f32 v[90:91], v[154:155], v[90:91]
	v_mov_b32_e32 v154, v63
	v_mov_b32_e32 v155, v55
	v_pk_mul_f32 v[92:93], v[152:153], v[92:93]
	s_waitcnt vmcnt(18)
	v_pk_add_f32 v[124:125], v[158:159], 1.0 op_sel_hi:[1,0]
	v_mov_b32_e32 v152, v62
	v_mov_b32_e32 v153, v54
	v_pk_mul_f32 v[154:155], v[154:155], v[154:155]
	v_mov_b32_e32 v158, v65
	v_mov_b32_e32 v159, v57
	v_pk_fma_f32 v[152:153], v[152:153], v[152:153], v[154:155]
	v_mov_b32_e32 v154, v64
	v_mov_b32_e32 v155, v56
	v_pk_mul_f32 v[158:159], v[158:159], v[158:159]
	v_pk_add_f32 v[156:157], v[156:157], 1.0 op_sel_hi:[1,0]
	v_pk_fma_f32 v[154:155], v[154:155], v[154:155], v[158:159]
	v_pk_mul_f32 v[158:159], v[46:47], v[46:47]
	v_pk_add_f32 v[152:153], v[152:153], v[154:155]
	v_pk_mul_f32 v[154:155], v[48:49], v[48:49]
	v_pk_add_f32 v[152:153], v[152:153], v[152:153] op_sel:[0,1] op_sel_hi:[1,0]
	v_pk_mov_b32 v[160:161], v[158:159], v[154:155] op_sel:[1,0]
	v_mov_b32_e32 v159, v155
	v_pk_add_f32 v[154:155], v[160:161], v[158:159]
	v_mul_f32_e32 v158, v31, v31
	v_pk_add_f32 v[154:155], v[154:155], v[154:155] op_sel:[0,1] op_sel_hi:[1,0]
	v_mov_b32_e32 v153, v139
	v_mov_b32_e32 v155, v158
	v_pk_add_f32 v[152:153], v[152:153], v[154:155]
	v_mul_f32_e32 v154, v39, v39
	v_mul_f32_e32 v159, v32, v32
	v_pk_fma_f32 v[154:155], v[38:39], v[38:39], v[154:155] op_sel_hi:[1,1,0]
	v_mul_f32_e32 v158, v41, v41
	v_mul_f32_e32 v160, v33, v33
	v_mov_b32_e32 v155, v159
	v_pk_fma_f32 v[158:159], v[40:41], v[40:41], v[158:159] op_sel_hi:[1,1,0]
	v_mul_f32_e32 v139, v6, v6
	v_mov_b32_e32 v159, v160
	v_pk_add_f32 v[154:155], v[154:155], v[158:159]
	v_pk_mul_f32 v[158:159], v[22:23], v[22:23]
	v_pk_add_f32 v[152:153], v[152:153], v[154:155]
	v_pk_mul_f32 v[154:155], v[24:25], v[24:25]
	v_pk_add_f32 v[152:153], v[152:153], v[152:153] op_sel:[0,1] op_sel_hi:[1,0]
	v_pk_mov_b32 v[160:161], v[158:159], v[154:155] op_sel:[1,0]
	v_mov_b32_e32 v159, v155
	v_pk_add_f32 v[154:155], v[160:161], v[158:159]
	v_mul_f32_e32 v158, v7, v7
	v_pk_add_f32 v[154:155], v[154:155], v[154:155] op_sel:[0,1] op_sel_hi:[1,0]
	v_mov_b32_e32 v153, v139
	v_mov_b32_e32 v155, v158
	v_pk_add_f32 v[152:153], v[152:153], v[154:155]
	v_mul_f32_e32 v154, v15, v15
	v_mul_f32_e32 v159, v8, v8
	v_pk_fma_f32 v[154:155], v[14:15], v[14:15], v[154:155] op_sel_hi:[1,1,0]
	v_mul_f32_e32 v158, v17, v17
	v_mul_f32_e32 v160, v9, v9
	v_mov_b32_e32 v155, v159
	v_pk_fma_f32 v[158:159], v[16:17], v[16:17], v[158:159] op_sel_hi:[1,1,0]
	s_waitcnt vmcnt(17)
	v_mov_b32_e32 v161, v53
	v_mov_b32_e32 v159, v160
	v_pk_add_f32 v[154:155], v[154:155], v[158:159]
	s_waitcnt vmcnt(14)
	v_mov_b32_e32 v158, v59
	v_mov_b32_e32 v159, v51
	v_pk_add_f32 v[152:153], v[152:153], v[154:155]
	v_mov_b32_e32 v154, v58
	v_mov_b32_e32 v155, v50
	v_pk_mul_f32 v[158:159], v[158:159], v[158:159]
	v_mov_b32_e32 v160, v61
	v_pk_fma_f32 v[154:155], v[154:155], v[154:155], v[158:159]
	v_mov_b32_e32 v158, v60
	v_mov_b32_e32 v159, v52
	v_pk_mul_f32 v[160:161], v[160:161], v[160:161]
	s_waitcnt vmcnt(13)
	v_mul_f32_e32 v139, v26, v26
	v_pk_fma_f32 v[158:159], v[158:159], v[158:159], v[160:161]
	v_pk_mul_f32 v[160:161], v[42:43], v[42:43]
	v_pk_add_f32 v[154:155], v[154:155], v[158:159]
	v_pk_mul_f32 v[158:159], v[44:45], v[44:45]
	v_pk_add_f32 v[154:155], v[154:155], v[154:155] op_sel:[0,1] op_sel_hi:[1,0]
	v_pk_mov_b32 v[162:163], v[160:161], v[158:159] op_sel:[1,0]
	v_mov_b32_e32 v161, v159
	v_pk_add_f32 v[158:159], v[162:163], v[160:161]
	v_mul_f32_e32 v160, v27, v27
	v_pk_add_f32 v[158:159], v[158:159], v[158:159] op_sel:[0,1] op_sel_hi:[1,0]
	v_mov_b32_e32 v155, v139
	v_mov_b32_e32 v159, v160
	v_pk_add_f32 v[154:155], v[154:155], v[158:159]
	v_mul_f32_e32 v158, v35, v35
	v_mul_f32_e32 v161, v28, v28
	v_pk_fma_f32 v[158:159], v[34:35], v[34:35], v[158:159] op_sel_hi:[1,1,0]
	v_mul_f32_e32 v160, v37, v37
	v_mul_f32_e32 v162, v29, v29
	v_mov_b32_e32 v159, v161
	v_pk_fma_f32 v[160:161], v[36:37], v[36:37], v[160:161] op_sel_hi:[1,1,0]
	s_waitcnt vmcnt(10)
	v_mul_f32_e32 v139, v2, v2
	v_mov_b32_e32 v161, v162
	v_pk_add_f32 v[158:159], v[158:159], v[160:161]
	v_pk_mul_f32 v[160:161], v[18:19], v[18:19]
	v_pk_add_f32 v[154:155], v[154:155], v[158:159]
	v_pk_mul_f32 v[158:159], v[20:21], v[20:21]
	v_pk_add_f32 v[154:155], v[154:155], v[154:155] op_sel:[0,1] op_sel_hi:[1,0]
	v_pk_mov_b32 v[162:163], v[160:161], v[158:159] op_sel:[1,0]
	v_mov_b32_e32 v161, v159
	v_pk_add_f32 v[158:159], v[162:163], v[160:161]
	v_mul_f32_e32 v160, v3, v3
	v_pk_add_f32 v[158:159], v[158:159], v[158:159] op_sel:[0,1] op_sel_hi:[1,0]
	v_mov_b32_e32 v155, v139
	v_mov_b32_e32 v159, v160
	v_pk_add_f32 v[154:155], v[154:155], v[158:159]
	v_mul_f32_e32 v158, v11, v11
	v_mul_f32_e32 v161, v4, v4
	v_pk_fma_f32 v[158:159], v[10:11], v[10:11], v[158:159] op_sel_hi:[1,1,0]
	v_mul_f32_e32 v160, v13, v13
	v_mul_f32_e32 v162, v5, v5
	v_mov_b32_e32 v159, v161
	v_pk_fma_f32 v[160:161], v[12:13], v[12:13], v[160:161] op_sel_hi:[1,1,0]
	s_waitcnt vmcnt(4)
	v_pk_mul_f32 v[124:125], v[122:123], v[124:125]
	v_mov_b32_e32 v161, v162
	v_pk_add_f32 v[158:159], v[158:159], v[160:161]
	v_pk_mul_f32 v[156:157], v[120:121], v[156:157]
	v_pk_add_f32 v[154:155], v[154:155], v[158:159]
	v_mov_b32_e32 v159, v152
	v_mov_b32_e32 v158, v154
	v_mov_b32_e32 v152, v155
	v_pk_add_f32 v[158:159], v[158:159], v[152:153]
	global_load_dwordx4 v[152:155], v127, s[14:15]
	global_load_dwordx4 v[120:123], v131, s[14:15]
	ds_bpermute_b32 v161, v138, v159
	ds_bpermute_b32 v160, v138, v158
	s_waitcnt vmcnt(3)
	v_pk_add_f32 v[146:147], v[146:147], 1.0 op_sel_hi:[1,0]
	v_pk_add_f32 v[144:145], v[144:145], 1.0 op_sel_hi:[1,0]
	v_pk_mul_f32 v[146:147], v[142:143], v[146:147]
	v_pk_mul_f32 v[144:145], v[140:141], v[144:145]
	global_load_dwordx4 v[140:143], v128, s[14:15]
	s_waitcnt lgkmcnt(0)
	v_pk_add_f32 v[158:159], v[158:159], v[160:161]
	ds_bpermute_b32 v161, v137, v159
	ds_bpermute_b32 v160, v137, v158
	v_pk_add_f32 v[88:89], v[88:89], 1.0 op_sel_hi:[1,0]
	v_pk_add_f32 v[86:87], v[86:87], 1.0 op_sel_hi:[1,0]
	s_waitcnt vmcnt(3)
	v_pk_mul_f32 v[88:89], v[150:151], v[88:89]
	v_pk_mul_f32 v[148:149], v[148:149], v[86:87]
	s_waitcnt lgkmcnt(0)
	v_pk_add_f32 v[158:159], v[158:159], v[160:161]
	ds_bpermute_b32 v161, v136, v159
	ds_bpermute_b32 v160, v136, v158
	s_waitcnt lgkmcnt(0)
	v_pk_add_f32 v[150:151], v[158:159], v[160:161]
	ds_bpermute_b32 v159, v135, v151
	ds_bpermute_b32 v158, v135, v150
	v_lshl_add_u64 v[160:161], v[100:101], 0, s[10:11]
	s_add_i32 s10, s1, s0
	s_lshr_b32 s1, s10, 11
	s_mul_i32 s12, s1, 0x3000
	s_waitcnt lgkmcnt(0)
	v_pk_add_f32 v[86:87], v[150:151], v[158:159]
	ds_bpermute_b32 v151, v134, v87
	ds_bpermute_b32 v150, v134, v86
	s_ashr_i32 s11, s10, 31
	s_ashr_i32 s13, s12, 31
	s_lshl_b64 s[14:15], s[10:11], 13
	s_lshl_b64 s[12:13], s[12:13], 2
	s_waitcnt lgkmcnt(0)
	v_pk_add_f32 v[86:87], v[86:87], v[150:151]
	ds_bpermute_b32 v151, v133, v87
	ds_bpermute_b32 v150, v133, v86
	s_add_u32 s12, s3, s12
	s_addc_u32 s13, s2, s13
	s_add_u32 s16, s12, 0x2000
	s_addc_u32 s17, s13, 0
	s_waitcnt lgkmcnt(0)
	v_pk_add_f32 v[86:87], v[86:87], v[150:151]
	s_mov_b32 s1, 0x1001000
	v_pk_fma_f32 v[86:87], v[86:87], s[8:9], v[104:105] op_sel_hi:[1,0,0]
	s_lshl_b64 s[10:11], s[10:11], 11
	v_mul_f32_e32 v139, 0x4b800000, v87
	v_cmp_gt_f32_e32 vcc, s23, v87
	s_nop 1
	v_cndmask_b32_e32 v87, v87, v139, vcc
	v_rsq_f32_e32 v87, v87
	s_nop 0
	v_mul_f32_e32 v139, 0x45800000, v87
	v_cndmask_b32_e32 v150, v87, v139, vcc
	v_pk_mul_f32 v[62:63], v[62:63], v[150:151] op_sel_hi:[1,0]
	v_pk_mul_f32 v[64:65], v[64:65], v[150:151] op_sel_hi:[1,0]
	v_pk_fma_f32 v[62:63], v[112:113], v[62:63], v[82:83]
	v_mov_b32_e32 v82, v99
	v_med3_f32 v62, v62, s22, v132
	v_med3_f32 v63, v63, s22, v132
	v_cvt_pk_fp8_f32 v82, v62, v63
	v_pk_fma_f32 v[62:63], v[108:109], v[64:65], v[84:85]
	v_pk_mul_f32 v[54:55], v[54:55], v[150:151] op_sel_hi:[1,0]
	v_med3_f32 v62, v62, s22, v132
	v_med3_f32 v63, v63, s22, v132
	v_pk_fma_f32 v[54:55], v[118:119], v[54:55], v[78:79]
	v_cvt_pk_fp8_f32 v82, v62, v63 op_sel:[0,0,1]
	v_med3_f32 v54, v54, s22, v132
	v_med3_f32 v55, v55, s22, v132
	v_mov_b32_e32 v62, v99
	v_cvt_pk_fp8_f32 v62, v54, v55
	v_pk_mul_f32 v[56:57], v[56:57], v[150:151] op_sel_hi:[1,0]
	v_pk_mul_f32 v[46:47], v[46:47], v[150:151] op_sel_hi:[1,0]
	v_pk_fma_f32 v[54:55], v[116:117], v[56:57], v[80:81]
	v_pk_fma_f32 v[46:47], v[114:115], v[46:47], v[74:75]
	v_med3_f32 v54, v54, s22, v132
	v_med3_f32 v55, v55, s22, v132
	v_cvt_pk_fp8_f32 v62, v54, v55 op_sel:[0,0,1]
	v_med3_f32 v46, v46, s22, v132
	v_med3_f32 v47, v47, s22, v132
	v_mov_b32_e32 v54, v99
	v_cvt_pk_fp8_f32 v54, v46, v47
	v_pk_mul_f32 v[48:49], v[48:49], v[150:151] op_sel_hi:[1,0]
	v_pk_mul_f32 v[38:39], v[38:39], v[150:151] op_sel_hi:[1,0]
	v_pk_fma_f32 v[46:47], v[110:111], v[48:49], v[76:77]
	v_pk_fma_f32 v[38:39], v[106:107], v[38:39], v[70:71]
	v_med3_f32 v46, v46, s22, v132
	v_med3_f32 v47, v47, s22, v132
	v_cvt_pk_fp8_f32 v54, v46, v47 op_sel:[0,0,1]
	v_med3_f32 v38, v38, s22, v132
	v_med3_f32 v39, v39, s22, v132
	v_mov_b32_e32 v46, v99
	v_cvt_pk_fp8_f32 v46, v38, v39
	v_pk_mul_f32 v[40:41], v[40:41], v[150:151] op_sel_hi:[1,0]
	v_pk_mul_f32 v[30:31], v[30:31], v[150:151] op_sel_hi:[1,0]
	v_pk_fma_f32 v[38:39], v[96:97], v[40:41], v[72:73]
	v_pk_fma_f32 v[30:31], v[92:93], v[30:31], v[66:67]
	v_med3_f32 v38, v38, s22, v132
	v_med3_f32 v39, v39, s22, v132
	v_cvt_pk_fp8_f32 v46, v38, v39 op_sel:[0,0,1]
	v_med3_f32 v30, v30, s22, v132
	v_med3_f32 v31, v31, s22, v132
	v_mov_b32_e32 v38, v99
	v_cvt_pk_fp8_f32 v38, v30, v31
	v_pk_mul_f32 v[32:33], v[32:33], v[150:151] op_sel_hi:[1,0]
	v_pk_mul_f32 v[22:23], v[22:23], v[150:151] op_sel_hi:[1,0]
	v_pk_fma_f32 v[30:31], v[90:91], v[32:33], v[68:69]
	s_waitcnt vmcnt(2)
	v_pk_fma_f32 v[22:23], v[156:157], v[22:23], v[152:153]
	v_med3_f32 v30, v30, s22, v132
	v_med3_f32 v31, v31, s22, v132
	v_cvt_pk_fp8_f32 v38, v30, v31 op_sel:[0,0,1]
	v_med3_f32 v22, v22, s22, v132
	v_med3_f32 v23, v23, s22, v132
	v_mov_b32_e32 v30, v99
	v_cvt_pk_fp8_f32 v30, v22, v23
	v_pk_mul_f32 v[24:25], v[24:25], v[150:151] op_sel_hi:[1,0]
	v_pk_mul_f32 v[14:15], v[14:15], v[150:151] op_sel_hi:[1,0]
	v_pk_fma_f32 v[22:23], v[124:125], v[24:25], v[154:155]
	s_waitcnt vmcnt(1)
	v_pk_fma_f32 v[14:15], v[144:145], v[14:15], v[120:121]
	v_med3_f32 v22, v22, s22, v132
	v_med3_f32 v23, v23, s22, v132
	v_cvt_pk_fp8_f32 v30, v22, v23 op_sel:[0,0,1]
	v_med3_f32 v14, v14, s22, v132
	v_med3_f32 v15, v15, s22, v132
	v_mov_b32_e32 v22, v99
	v_cvt_pk_fp8_f32 v22, v14, v15
	v_pk_mul_f32 v[16:17], v[16:17], v[150:151] op_sel_hi:[1,0]
	v_pk_mul_f32 v[6:7], v[6:7], v[150:151] op_sel_hi:[1,0]
	v_pk_fma_f32 v[14:15], v[146:147], v[16:17], v[122:123]
	s_waitcnt vmcnt(0)
	v_pk_fma_f32 v[6:7], v[148:149], v[6:7], v[140:141]
	v_med3_f32 v14, v14, s22, v132
	v_med3_f32 v15, v15, s22, v132
	v_cvt_pk_fp8_f32 v22, v14, v15 op_sel:[0,0,1]
	v_med3_f32 v6, v6, s22, v132
	v_med3_f32 v7, v7, s22, v132
	v_mov_b32_e32 v14, v99
	v_cvt_pk_fp8_f32 v14, v6, v7
	v_pk_mul_f32 v[8:9], v[8:9], v[150:151] op_sel_hi:[1,0]
	global_store_dword v[160:161], v82, off
	global_store_dword v[160:161], v62, off offset:256
	global_store_dword v[160:161], v54, off offset:512
	global_store_dword v[160:161], v46, off offset:768
	v_pk_fma_f32 v[6:7], v[88:89], v[8:9], v[142:143]
	s_nop 0
	v_med3_f32 v6, v6, s22, v132
	v_med3_f32 v7, v7, s22, v132
	v_cvt_pk_fp8_f32 v14, v6, v7 op_sel:[0,0,1]
	global_store_dword v[160:161], v38, off offset:1024
	global_store_dword v[160:161], v30, off offset:1280
	global_store_dword v[160:161], v22, off offset:1536
	global_store_dword v[160:161], v14, off offset:1792
	global_load_dwordx4 v[66:69], v98, s[16:17]
	global_load_dwordx4 v[70:73], v98, s[6:7]
	global_load_dwordx4 v[74:77], v1, s[16:17]
	global_load_dwordx4 v[78:81], v98, s[6:7] offset:1024
	global_load_dwordx4 v[82:85], v129, s[16:17]
	global_load_dwordx4 v[88:91], v98, s[6:7] offset:2048
	global_load_dwordx4 v[106:109], v130, s[16:17]
	global_load_dwordx4 v[110:113], v98, s[6:7] offset:3072
	global_load_dwordx4 v[114:117], v126, s[16:17]
	global_load_dwordx4 v[118:121], v126, s[6:7]
	global_load_dwordx4 v[122:125], v127, s[16:17]
	global_load_dwordx4 v[140:143], v127, s[6:7]
	global_load_dwordx4 v[144:147], v131, s[16:17]
	global_load_dwordx4 v[148:151], v131, s[6:7]
	global_load_dwordx4 v[152:155], v128, s[16:17]
	global_load_dwordx4 v[156:159], v128, s[6:7]
	global_load_dwordx4 v[160:163], v98, s[12:13]
	global_load_dwordx4 v[164:167], v98, s[12:13] offset:1024
	global_load_dwordx4 v[168:171], v98, s[12:13] offset:2048
	v_lshl_add_u64 v[6:7], v[102:103], 0, s[14:15]
	s_mov_b64 s[14:15], 0x1000000
	v_lshl_add_u64 v[8:9], v[6:7], 0, s[14:15]
	v_add_co_u32_e32 v6, vcc, s1, v6
	s_mov_b64 s[16:17], 0x5000000
	s_nop 0
	v_addc_co_u32_e32 v7, vcc, 0, v7, vcc
	global_load_dwordx4 v[54:57], v[8:9], off offset:1024 nt
	global_load_dwordx4 v[46:49], v[8:9], off offset:2048 nt
	global_load_dwordx4 v[38:41], v[8:9], off offset:3072 nt
	global_load_dwordx4 v[62:65], v[6:7], off offset:-4096
	global_load_dwordx4 v[30:33], v[6:7], off nt
	global_load_dwordx4 v[22:25], v[6:7], off offset:1024 nt
	global_load_dwordx4 v[14:17], v[6:7], off offset:2048 nt
	s_nop 0
	global_load_dwordx4 v[6:9], v[6:7], off offset:3072 nt
	s_nop 0
	global_load_dwordx4 v[172:175], v98, s[12:13] offset:3072
	v_cmp_gt_f32_e32 vcc, s23, v86
	s_waitcnt vmcnt(27)
	v_pk_add_f32 v[68:69], v[68:69], 1.0 op_sel_hi:[1,0]
	v_pk_add_f32 v[66:67], v[66:67], 1.0 op_sel_hi:[1,0]
	s_waitcnt vmcnt(26)
	v_pk_mul_f32 v[92:93], v[72:73], v[68:69]
	v_pk_mul_f32 v[96:97], v[70:71], v[66:67]
	s_waitcnt vmcnt(25)
	v_pk_add_f32 v[66:67], v[76:77], 1.0 op_sel_hi:[1,0]
	v_pk_add_f32 v[68:69], v[74:75], 1.0 op_sel_hi:[1,0]
	s_waitcnt vmcnt(24)
	v_pk_mul_f32 v[176:177], v[80:81], v[66:67]
	v_pk_mul_f32 v[178:179], v[78:79], v[68:69]
	s_waitcnt vmcnt(23)
	v_pk_add_f32 v[66:67], v[84:85], 1.0 op_sel_hi:[1,0]
	v_pk_add_f32 v[68:69], v[82:83], 1.0 op_sel_hi:[1,0]
	s_waitcnt vmcnt(22)
	v_pk_mul_f32 v[82:83], v[90:91], v[66:67]
	v_pk_mul_f32 v[84:85], v[88:89], v[68:69]
	global_load_dwordx4 v[66:69], v126, s[12:13]
	s_waitcnt vmcnt(22)
	v_pk_add_f32 v[70:71], v[108:109], 1.0 op_sel_hi:[1,0]
	v_pk_add_f32 v[72:73], v[106:107], 1.0 op_sel_hi:[1,0]
	s_waitcnt vmcnt(21)
	v_pk_mul_f32 v[88:89], v[112:113], v[70:71]
	v_pk_mul_f32 v[90:91], v[110:111], v[72:73]
	s_waitcnt vmcnt(20)
	v_pk_add_f32 v[70:71], v[116:117], 1.0 op_sel_hi:[1,0]
	v_pk_add_f32 v[72:73], v[114:115], 1.0 op_sel_hi:[1,0]
	s_waitcnt vmcnt(19)
	v_pk_mul_f32 v[106:107], v[120:121], v[70:71]
	v_pk_mul_f32 v[108:109], v[118:119], v[72:73]
	global_load_dwordx4 v[70:73], v127, s[12:13]
	s_waitcnt vmcnt(19)
	v_pk_add_f32 v[74:75], v[124:125], 1.0 op_sel_hi:[1,0]
	v_pk_add_f32 v[76:77], v[122:123], 1.0 op_sel_hi:[1,0]
	s_waitcnt vmcnt(18)
	v_pk_mul_f32 v[110:111], v[142:143], v[74:75]
	v_pk_mul_f32 v[112:113], v[140:141], v[76:77]
	global_load_dwordx4 v[74:77], v131, s[12:13]
	s_waitcnt vmcnt(18)
	v_pk_add_f32 v[78:79], v[146:147], 1.0 op_sel_hi:[1,0]
	v_pk_add_f32 v[80:81], v[144:145], 1.0 op_sel_hi:[1,0]
	s_waitcnt vmcnt(17)
	v_pk_mul_f32 v[114:115], v[150:151], v[78:79]
	v_mul_f32_e32 v78, 0x4b800000, v86
	v_cndmask_b32_e32 v78, v86, v78, vcc
	v_pk_mul_f32 v[116:117], v[148:149], v[80:81]
	v_rsq_f32_e32 v122, v78
	global_load_dwordx4 v[78:81], v128, s[12:13]
	s_waitcnt vmcnt(17)
	v_pk_add_f32 v[118:119], v[154:155], 1.0 op_sel_hi:[1,0]
	v_pk_add_f32 v[120:121], v[152:153], 1.0 op_sel_hi:[1,0]
	s_waitcnt vmcnt(16)
	v_pk_mul_f32 v[86:87], v[158:159], v[118:119]
	v_pk_mul_f32 v[118:119], v[156:157], v[120:121]
	v_mul_f32_e32 v120, 0x45800000, v122
	v_cndmask_b32_e32 v120, v122, v120, vcc
	v_pk_mul_f32 v[58:59], v[58:59], v[120:121] op_sel_hi:[1,0]
	v_pk_mul_f32 v[60:61], v[60:61], v[120:121] op_sel_hi:[1,0]
	s_waitcnt vmcnt(15)
	v_pk_fma_f32 v[58:59], v[96:97], v[58:59], v[160:161]
	v_mov_b32_e32 v96, v99
	v_med3_f32 v58, v58, s22, v132
	v_med3_f32 v59, v59, s22, v132
	v_cvt_pk_fp8_f32 v96, v58, v59
	v_pk_fma_f32 v[58:59], v[92:93], v[60:61], v[162:163]
	v_pk_mul_f32 v[50:51], v[50:51], v[120:121] op_sel_hi:[1,0]
	v_med3_f32 v58, v58, s22, v132
	v_med3_f32 v59, v59, s22, v132
	s_waitcnt vmcnt(14)
	v_pk_fma_f32 v[50:51], v[178:179], v[50:51], v[164:165]
	v_cvt_pk_fp8_f32 v96, v58, v59 op_sel:[0,0,1]
	v_med3_f32 v50, v50, s22, v132
	v_med3_f32 v51, v51, s22, v132
	v_mov_b32_e32 v58, v99
	v_cvt_pk_fp8_f32 v58, v50, v51
	v_pk_mul_f32 v[52:53], v[52:53], v[120:121] op_sel_hi:[1,0]
	v_pk_mul_f32 v[42:43], v[42:43], v[120:121] op_sel_hi:[1,0]
	v_pk_fma_f32 v[50:51], v[176:177], v[52:53], v[166:167]
	s_waitcnt vmcnt(13)
	v_pk_fma_f32 v[42:43], v[84:85], v[42:43], v[168:169]
	v_med3_f32 v50, v50, s22, v132
	v_med3_f32 v51, v51, s22, v132
	v_cvt_pk_fp8_f32 v58, v50, v51 op_sel:[0,0,1]
	v_med3_f32 v42, v42, s22, v132
	v_med3_f32 v43, v43, s22, v132
	v_mov_b32_e32 v50, v99
	v_cvt_pk_fp8_f32 v50, v42, v43
	v_pk_mul_f32 v[44:45], v[44:45], v[120:121] op_sel_hi:[1,0]
	v_pk_mul_f32 v[34:35], v[34:35], v[120:121] op_sel_hi:[1,0]
	v_pk_fma_f32 v[42:43], v[82:83], v[44:45], v[170:171]
	s_waitcnt vmcnt(4)
	v_pk_fma_f32 v[34:35], v[90:91], v[34:35], v[172:173]
	v_med3_f32 v42, v42, s22, v132
	v_med3_f32 v43, v43, s22, v132
	v_cvt_pk_fp8_f32 v50, v42, v43 op_sel:[0,0,1]
	v_med3_f32 v34, v34, s22, v132
	v_med3_f32 v35, v35, s22, v132
	v_mov_b32_e32 v42, v99
	v_cvt_pk_fp8_f32 v42, v34, v35
	v_pk_mul_f32 v[36:37], v[36:37], v[120:121] op_sel_hi:[1,0]
	v_pk_mul_f32 v[26:27], v[26:27], v[120:121] op_sel_hi:[1,0]
	v_pk_fma_f32 v[34:35], v[88:89], v[36:37], v[174:175]
	v_pk_mul_f32 v[28:29], v[28:29], v[120:121] op_sel_hi:[1,0]
	v_med3_f32 v34, v34, s22, v132
	v_med3_f32 v35, v35, s22, v132
	v_cvt_pk_fp8_f32 v42, v34, v35 op_sel:[0,0,1]
	v_mov_b32_e32 v34, v99
	v_pk_mul_f32 v[18:19], v[18:19], v[120:121] op_sel_hi:[1,0]
	v_pk_mul_f32 v[20:21], v[20:21], v[120:121] op_sel_hi:[1,0]
	v_pk_mul_f32 v[10:11], v[10:11], v[120:121] op_sel_hi:[1,0]
	v_pk_mul_f32 v[12:13], v[12:13], v[120:121] op_sel_hi:[1,0]
	s_waitcnt vmcnt(3)
	v_pk_fma_f32 v[26:27], v[108:109], v[26:27], v[66:67]
	v_lshl_add_u64 v[122:123], v[100:101], 0, s[10:11]
	v_med3_f32 v26, v26, s22, v132
	v_med3_f32 v27, v27, s22, v132
	v_cvt_pk_fp8_f32 v34, v26, v27
	v_pk_fma_f32 v[26:27], v[106:107], v[28:29], v[68:69]
	v_pk_mul_f32 v[2:3], v[2:3], v[120:121] op_sel_hi:[1,0]
	v_med3_f32 v26, v26, s22, v132
	v_med3_f32 v27, v27, s22, v132
	s_waitcnt vmcnt(2)
	v_pk_fma_f32 v[18:19], v[112:113], v[18:19], v[70:71]
	v_cvt_pk_fp8_f32 v34, v26, v27 op_sel:[0,0,1]
	v_med3_f32 v18, v18, s22, v132
	v_med3_f32 v19, v19, s22, v132
	v_mov_b32_e32 v26, v99
	v_cvt_pk_fp8_f32 v26, v18, v19
	v_pk_fma_f32 v[18:19], v[110:111], v[20:21], v[72:73]
	s_waitcnt vmcnt(1)
	v_pk_fma_f32 v[10:11], v[116:117], v[10:11], v[74:75]
	v_med3_f32 v18, v18, s22, v132
	v_med3_f32 v19, v19, s22, v132
	v_cvt_pk_fp8_f32 v26, v18, v19 op_sel:[0,0,1]
	v_med3_f32 v10, v10, s22, v132
	v_med3_f32 v11, v11, s22, v132
	v_mov_b32_e32 v18, v99
	v_cvt_pk_fp8_f32 v18, v10, v11
	v_pk_fma_f32 v[10:11], v[114:115], v[12:13], v[76:77]
	s_add_i32 s10, s0, 0x2000
	v_med3_f32 v10, v10, s22, v132
	v_med3_f32 v11, v11, s22, v132
	s_waitcnt vmcnt(0)
	v_pk_fma_f32 v[2:3], v[118:119], v[2:3], v[78:79]
	s_lshr_b32 s1, s10, 11
	v_cvt_pk_fp8_f32 v18, v10, v11 op_sel:[0,0,1]
	v_med3_f32 v2, v2, s22, v132
	v_med3_f32 v3, v3, s22, v132
	v_mov_b32_e32 v10, v99
	s_mul_i32 s12, s1, 0x3000
	v_cvt_pk_fp8_f32 v10, v2, v3
	s_ashr_i32 s13, s12, 31
	v_pk_mul_f32 v[4:5], v[4:5], v[120:121] op_sel_hi:[1,0]
	s_lshl_b64 s[12:13], s[12:13], 2
	v_pk_fma_f32 v[2:3], v[86:87], v[4:5], v[80:81]
	s_add_u32 s12, s3, s12
	v_med3_f32 v2, v2, s22, v132
	v_med3_f32 v3, v3, s22, v132
	s_addc_u32 s13, s2, s13
	v_cvt_pk_fp8_f32 v10, v2, v3 op_sel:[0,0,1]
	s_add_u32 s14, s12, 0x2000
	global_store_dword v[122:123], v96, off
	global_store_dword v[122:123], v58, off offset:256
	global_store_dword v[122:123], v50, off offset:512
	global_store_dword v[122:123], v42, off offset:768
	global_store_dword v[122:123], v34, off offset:1024
	global_store_dword v[122:123], v26, off offset:1280
	global_store_dword v[122:123], v18, off offset:1536
	global_store_dword v[122:123], v10, off offset:1792
	s_addc_u32 s15, s13, 0
	global_load_dwordx4 v[66:69], v98, s[14:15]
	global_load_dwordx4 v[70:73], v98, s[6:7]
	global_load_dwordx4 v[74:77], v1, s[14:15]
	global_load_dwordx4 v[78:81], v98, s[6:7] offset:1024
	global_load_dwordx4 v[106:109], v129, s[14:15]
	global_load_dwordx4 v[110:113], v98, s[6:7] offset:2048
	global_load_dwordx4 v[140:143], v130, s[14:15]
	global_load_dwordx4 v[144:147], v98, s[6:7] offset:3072
	global_load_dwordx4 v[148:151], v126, s[14:15]
	global_load_dwordx4 v[152:155], v126, s[6:7]
	global_load_dwordx4 v[156:159], v127, s[14:15]
	global_load_dwordx4 v[90:93], v127, s[6:7]
	s_mov_b32 s1, 0x5001000
	v_add_co_u32_e32 v4, vcc, s1, v94
	v_lshl_add_u64 v[2:3], v[94:95], 0, s[16:17]
	s_nop 0
	v_addc_co_u32_e32 v5, vcc, 0, v95, vcc
	global_load_dwordx4 v[50:53], v[2:3], off offset:1024 nt
	global_load_dwordx4 v[42:45], v[2:3], off offset:2048 nt
	global_load_dwordx4 v[34:37], v[2:3], off offset:3072 nt
	global_load_dwordx4 v[58:61], v[4:5], off offset:-4096
	global_load_dwordx4 v[26:29], v[4:5], off nt
	global_load_dwordx4 v[18:21], v[4:5], off offset:1024 nt
	global_load_dwordx4 v[10:13], v[4:5], off offset:2048 nt
	s_nop 0
	global_load_dwordx4 v[2:5], v[4:5], off offset:3072 nt
	v_mul_f32_e32 v139, v30, v30
	global_load_dwordx4 v[94:97], v128, s[14:15]
	global_load_dwordx4 v[86:89], v98, s[12:13]
	global_load_dwordx4 v[82:85], v98, s[12:13] offset:1024
	s_ashr_i32 s11, s10, 31
	s_lshl_b64 s[10:11], s[10:11], 11
	s_mul_i32 s1, s81, 40
	s_waitcnt vmcnt(22)
	v_pk_add_f32 v[68:69], v[68:69], 1.0 op_sel_hi:[1,0]
	v_pk_add_f32 v[66:67], v[66:67], 1.0 op_sel_hi:[1,0]
	s_waitcnt vmcnt(21)
	v_pk_mul_f32 v[114:115], v[72:73], v[68:69]
	v_pk_mul_f32 v[118:119], v[70:71], v[66:67]
	s_waitcnt vmcnt(20)
	v_pk_add_f32 v[66:67], v[76:77], 1.0 op_sel_hi:[1,0]
	v_pk_add_f32 v[68:69], v[74:75], 1.0 op_sel_hi:[1,0]
	s_waitcnt vmcnt(19)
	v_pk_mul_f32 v[122:123], v[80:81], v[66:67]
	v_pk_mul_f32 v[124:125], v[78:79], v[68:69]
	s_waitcnt vmcnt(18)
	v_pk_add_f32 v[66:67], v[108:109], 1.0 op_sel_hi:[1,0]
	v_pk_add_f32 v[68:69], v[106:107], 1.0 op_sel_hi:[1,0]
	s_waitcnt vmcnt(17)
	v_pk_mul_f32 v[116:117], v[112:113], v[66:67]
	v_pk_mul_f32 v[120:121], v[110:111], v[68:69]
	s_waitcnt vmcnt(16)
	v_pk_add_f32 v[66:67], v[142:143], 1.0 op_sel_hi:[1,0]
	v_pk_add_f32 v[68:69], v[140:141], 1.0 op_sel_hi:[1,0]
	s_waitcnt vmcnt(15)
	v_pk_mul_f32 v[110:111], v[146:147], v[66:67]
	v_pk_mul_f32 v[112:113], v[144:145], v[68:69]
	s_waitcnt vmcnt(14)
	v_pk_add_f32 v[66:67], v[150:151], 1.0 op_sel_hi:[1,0]
	v_pk_add_f32 v[68:69], v[148:149], 1.0 op_sel_hi:[1,0]
	s_waitcnt vmcnt(12)
	v_pk_add_f32 v[140:141], v[158:159], 1.0 op_sel_hi:[1,0]
	global_load_dwordx4 v[78:81], v98, s[12:13] offset:2048
	global_load_dwordx4 v[74:77], v98, s[12:13] offset:3072
	global_load_dwordx4 v[70:73], v126, s[12:13]
	v_pk_mul_f32 v[106:107], v[154:155], v[66:67]
	v_pk_mul_f32 v[108:109], v[152:153], v[68:69]
	global_load_dwordx4 v[66:69], v127, s[12:13]
	s_waitcnt vmcnt(15)
	v_pk_mul_f32 v[92:93], v[92:93], v[140:141]
	global_load_dwordx4 v[140:143], v131, s[6:7]
	global_load_dwordx4 v[144:147], v131, s[14:15]
	global_load_dwordx4 v[148:151], v128, s[6:7]
	v_pk_add_f32 v[152:153], v[156:157], 1.0 op_sel_hi:[1,0]
	v_mov_b32_e32 v156, v63
	v_mov_b32_e32 v157, v55
	v_mov_b32_e32 v154, v62
	v_mov_b32_e32 v155, v54
	v_pk_mul_f32 v[156:157], v[156:157], v[156:157]
	v_mov_b32_e32 v158, v65
	v_mov_b32_e32 v159, v57
	v_pk_fma_f32 v[154:155], v[154:155], v[154:155], v[156:157]
	v_mov_b32_e32 v156, v64
	v_mov_b32_e32 v157, v56
	v_pk_mul_f32 v[158:159], v[158:159], v[158:159]
	v_pk_mul_f32 v[152:153], v[90:91], v[152:153]
	v_pk_fma_f32 v[156:157], v[156:157], v[156:157], v[158:159]
	v_pk_mul_f32 v[158:159], v[46:47], v[46:47]
	v_pk_add_f32 v[154:155], v[154:155], v[156:157]
	v_pk_mul_f32 v[156:157], v[48:49], v[48:49]
	v_pk_add_f32 v[154:155], v[154:155], v[154:155] op_sel:[0,1] op_sel_hi:[1,0]
	v_pk_mov_b32 v[160:161], v[158:159], v[156:157] op_sel:[1,0]
	v_mov_b32_e32 v159, v157
	v_pk_add_f32 v[156:157], v[160:161], v[158:159]
	v_mul_f32_e32 v158, v31, v31
	v_pk_add_f32 v[156:157], v[156:157], v[156:157] op_sel:[0,1] op_sel_hi:[1,0]
	v_mov_b32_e32 v155, v139
	v_mov_b32_e32 v157, v158
	v_pk_add_f32 v[154:155], v[154:155], v[156:157]
	v_mul_f32_e32 v156, v39, v39
	v_mul_f32_e32 v159, v32, v32
	v_pk_fma_f32 v[156:157], v[38:39], v[38:39], v[156:157] op_sel_hi:[1,1,0]
	v_mul_f32_e32 v158, v41, v41
	v_mul_f32_e32 v160, v33, v33
	v_mov_b32_e32 v157, v159
	v_pk_fma_f32 v[158:159], v[40:41], v[40:41], v[158:159] op_sel_hi:[1,1,0]
	v_mul_f32_e32 v139, v6, v6
	v_mov_b32_e32 v159, v160
	v_pk_add_f32 v[156:157], v[156:157], v[158:159]
	v_pk_mul_f32 v[158:159], v[22:23], v[22:23]
	v_pk_add_f32 v[154:155], v[154:155], v[156:157]
	v_pk_mul_f32 v[156:157], v[24:25], v[24:25]
	v_pk_add_f32 v[154:155], v[154:155], v[154:155] op_sel:[0,1] op_sel_hi:[1,0]
	v_pk_mov_b32 v[160:161], v[158:159], v[156:157] op_sel:[1,0]
	v_mov_b32_e32 v159, v157
	v_pk_add_f32 v[156:157], v[160:161], v[158:159]
	v_mul_f32_e32 v158, v7, v7
	v_pk_add_f32 v[156:157], v[156:157], v[156:157] op_sel:[0,1] op_sel_hi:[1,0]
	v_mov_b32_e32 v155, v139
	v_mov_b32_e32 v157, v158
	v_pk_add_f32 v[154:155], v[154:155], v[156:157]
	v_mul_f32_e32 v156, v15, v15
	v_mul_f32_e32 v159, v8, v8
	v_pk_fma_f32 v[156:157], v[14:15], v[14:15], v[156:157] op_sel_hi:[1,1,0]
	v_mul_f32_e32 v158, v17, v17
	v_mul_f32_e32 v160, v9, v9
	v_mov_b32_e32 v157, v159
	v_pk_fma_f32 v[158:159], v[16:17], v[16:17], v[158:159] op_sel_hi:[1,1,0]
	s_waitcnt vmcnt(17)
	v_mov_b32_e32 v161, v53
	v_mov_b32_e32 v159, v160
	v_pk_add_f32 v[156:157], v[156:157], v[158:159]
	s_waitcnt vmcnt(14)
	v_mov_b32_e32 v158, v59
	v_mov_b32_e32 v159, v51
	v_pk_add_f32 v[154:155], v[154:155], v[156:157]
	v_mov_b32_e32 v156, v58
	v_mov_b32_e32 v157, v50
	v_pk_mul_f32 v[158:159], v[158:159], v[158:159]
	v_mov_b32_e32 v160, v61
	v_pk_fma_f32 v[156:157], v[156:157], v[156:157], v[158:159]
	v_mov_b32_e32 v158, v60
	v_mov_b32_e32 v159, v52
	v_pk_mul_f32 v[160:161], v[160:161], v[160:161]
	s_waitcnt vmcnt(13)
	v_mul_f32_e32 v139, v26, v26
	v_pk_fma_f32 v[158:159], v[158:159], v[158:159], v[160:161]
	v_pk_mul_f32 v[160:161], v[42:43], v[42:43]
	v_pk_add_f32 v[156:157], v[156:157], v[158:159]
	v_pk_mul_f32 v[158:159], v[44:45], v[44:45]
	v_pk_add_f32 v[156:157], v[156:157], v[156:157] op_sel:[0,1] op_sel_hi:[1,0]
	v_pk_mov_b32 v[162:163], v[160:161], v[158:159] op_sel:[1,0]
	v_mov_b32_e32 v161, v159
	v_pk_add_f32 v[158:159], v[162:163], v[160:161]
	v_mul_f32_e32 v160, v27, v27
	v_pk_add_f32 v[158:159], v[158:159], v[158:159] op_sel:[0,1] op_sel_hi:[1,0]
	v_mov_b32_e32 v157, v139
	v_mov_b32_e32 v159, v160
	v_pk_add_f32 v[156:157], v[156:157], v[158:159]
	v_mul_f32_e32 v158, v35, v35
	v_mul_f32_e32 v161, v28, v28
	v_pk_fma_f32 v[158:159], v[34:35], v[34:35], v[158:159] op_sel_hi:[1,1,0]
	v_mul_f32_e32 v160, v37, v37
	v_mul_f32_e32 v162, v29, v29
	v_mov_b32_e32 v159, v161
	v_pk_fma_f32 v[160:161], v[36:37], v[36:37], v[160:161] op_sel_hi:[1,1,0]
	s_waitcnt vmcnt(10)
	v_mul_f32_e32 v139, v2, v2
	v_mov_b32_e32 v161, v162
	v_pk_add_f32 v[158:159], v[158:159], v[160:161]
	v_pk_mul_f32 v[160:161], v[18:19], v[18:19]
	v_pk_add_f32 v[156:157], v[156:157], v[158:159]
	v_pk_mul_f32 v[158:159], v[20:21], v[20:21]
	v_pk_add_f32 v[156:157], v[156:157], v[156:157] op_sel:[0,1] op_sel_hi:[1,0]
	v_pk_mov_b32 v[162:163], v[160:161], v[158:159] op_sel:[1,0]
	v_mov_b32_e32 v161, v159
	v_pk_add_f32 v[158:159], v[162:163], v[160:161]
	v_mul_f32_e32 v160, v3, v3
	v_pk_add_f32 v[158:159], v[158:159], v[158:159] op_sel:[0,1] op_sel_hi:[1,0]
	v_mov_b32_e32 v157, v139
	v_mov_b32_e32 v159, v160
	v_pk_add_f32 v[156:157], v[156:157], v[158:159]
	v_mul_f32_e32 v158, v11, v11
	v_mul_f32_e32 v161, v4, v4
	v_pk_fma_f32 v[158:159], v[10:11], v[10:11], v[158:159] op_sel_hi:[1,1,0]
	v_mul_f32_e32 v160, v13, v13
	v_mul_f32_e32 v162, v5, v5
	v_mov_b32_e32 v159, v161
	v_pk_fma_f32 v[160:161], v[12:13], v[12:13], v[160:161] op_sel_hi:[1,1,0]
	s_waitcnt vmcnt(1)
	v_pk_add_f32 v[90:91], v[146:147], 1.0 op_sel_hi:[1,0]
	v_mov_b32_e32 v161, v162
	v_pk_add_f32 v[158:159], v[158:159], v[160:161]
	v_pk_mul_f32 v[142:143], v[142:143], v[90:91]
	v_pk_add_f32 v[156:157], v[156:157], v[158:159]
	v_mov_b32_e32 v159, v154
	v_mov_b32_e32 v158, v156
	v_mov_b32_e32 v154, v157
	v_pk_add_f32 v[154:155], v[158:159], v[154:155]
	v_pk_add_f32 v[158:159], v[144:145], 1.0 op_sel_hi:[1,0]
	global_load_dwordx4 v[144:147], v131, s[12:13]
	ds_bpermute_b32 v157, v138, v155
	ds_bpermute_b32 v156, v138, v154
	v_pk_mul_f32 v[140:141], v[140:141], v[158:159]
	v_pk_add_f32 v[90:91], v[96:97], 1.0 op_sel_hi:[1,0]
	v_pk_add_f32 v[158:159], v[94:95], 1.0 op_sel_hi:[1,0]
	global_load_dwordx4 v[94:97], v128, s[12:13]
	s_waitcnt lgkmcnt(0)
	v_pk_add_f32 v[154:155], v[154:155], v[156:157]
	ds_bpermute_b32 v157, v137, v155
	ds_bpermute_b32 v156, v137, v154
	s_waitcnt vmcnt(2)
	v_pk_mul_f32 v[150:151], v[150:151], v[90:91]
	v_pk_mul_f32 v[148:149], v[148:149], v[158:159]
	s_waitcnt lgkmcnt(0)
	v_pk_add_f32 v[154:155], v[154:155], v[156:157]
	ds_bpermute_b32 v157, v136, v155
	ds_bpermute_b32 v156, v136, v154
	s_waitcnt lgkmcnt(0)
	v_pk_add_f32 v[90:91], v[154:155], v[156:157]
	ds_bpermute_b32 v155, v135, v91
	ds_bpermute_b32 v154, v135, v90
	v_lshl_add_u64 v[156:157], v[100:101], 0, s[10:11]
	s_add_i32 s10, s1, s0
	s_lshr_b32 s9, s10, 11
	s_add_i32 s0, s10, 0x800
	s_waitcnt lgkmcnt(0)
	v_pk_add_f32 v[90:91], v[90:91], v[154:155]
	ds_bpermute_b32 v155, v134, v91
	ds_bpermute_b32 v154, v134, v90
	s_mul_i32 s12, s9, 0x3000
	s_ashr_i32 s1, s0, 31
	s_ashr_i32 s13, s12, 31
	s_lshl_b64 s[14:15], s[0:1], 13
	s_waitcnt lgkmcnt(0)
	v_pk_add_f32 v[90:91], v[90:91], v[154:155]
	ds_bpermute_b32 v155, v133, v91
	ds_bpermute_b32 v154, v133, v90
	s_lshl_b64 s[12:13], s[12:13], 2
	s_add_u32 s12, s3, s12
	s_addc_u32 s13, s2, s13
	s_add_u32 s16, s12, 0x2000
	s_waitcnt lgkmcnt(0)
	v_pk_add_f32 v[90:91], v[90:91], v[154:155]
	s_addc_u32 s17, s13, 0
	v_pk_fma_f32 v[90:91], v[90:91], s[8:9], v[104:105] op_sel_hi:[1,0,0]
	s_ashr_i32 s11, s10, 31
	v_mul_f32_e32 v139, 0x4b800000, v91
	v_cmp_gt_f32_e32 vcc, s23, v91
	s_lshr_b32 s9, s0, 11
	s_nop 0
	v_cndmask_b32_e32 v91, v91, v139, vcc
	v_rsq_f32_e32 v91, v91
	s_nop 0
	v_mul_f32_e32 v139, 0x45800000, v91
	v_cndmask_b32_e32 v154, v91, v139, vcc
	v_pk_mul_f32 v[62:63], v[62:63], v[154:155] op_sel_hi:[1,0]
	v_pk_mul_f32 v[64:65], v[64:65], v[154:155] op_sel_hi:[1,0]
	v_pk_fma_f32 v[62:63], v[118:119], v[62:63], v[86:87]
	v_mov_b32_e32 v86, v99
	v_med3_f32 v62, v62, s22, v132
	v_med3_f32 v63, v63, s22, v132
	v_cvt_pk_fp8_f32 v86, v62, v63
	v_pk_fma_f32 v[62:63], v[114:115], v[64:65], v[88:89]
	v_pk_mul_f32 v[54:55], v[54:55], v[154:155] op_sel_hi:[1,0]
	v_med3_f32 v62, v62, s22, v132
	v_med3_f32 v63, v63, s22, v132
	v_pk_fma_f32 v[54:55], v[124:125], v[54:55], v[82:83]
	v_cvt_pk_fp8_f32 v86, v62, v63 op_sel:[0,0,1]
	v_med3_f32 v54, v54, s22, v132
	v_med3_f32 v55, v55, s22, v132
	v_mov_b32_e32 v62, v99
	v_cvt_pk_fp8_f32 v62, v54, v55
	v_pk_mul_f32 v[56:57], v[56:57], v[154:155] op_sel_hi:[1,0]
	v_pk_mul_f32 v[46:47], v[46:47], v[154:155] op_sel_hi:[1,0]
	v_pk_fma_f32 v[54:55], v[122:123], v[56:57], v[84:85]
	v_pk_fma_f32 v[46:47], v[120:121], v[46:47], v[78:79]
	v_med3_f32 v54, v54, s22, v132
	v_med3_f32 v55, v55, s22, v132
	v_cvt_pk_fp8_f32 v62, v54, v55 op_sel:[0,0,1]
	v_med3_f32 v46, v46, s22, v132
	v_med3_f32 v47, v47, s22, v132
	v_mov_b32_e32 v54, v99
	v_cvt_pk_fp8_f32 v54, v46, v47
	v_pk_mul_f32 v[48:49], v[48:49], v[154:155] op_sel_hi:[1,0]
	v_pk_mul_f32 v[38:39], v[38:39], v[154:155] op_sel_hi:[1,0]
	v_pk_fma_f32 v[46:47], v[116:117], v[48:49], v[80:81]
	v_pk_fma_f32 v[38:39], v[112:113], v[38:39], v[74:75]
	v_med3_f32 v46, v46, s22, v132
	v_med3_f32 v47, v47, s22, v132
	v_cvt_pk_fp8_f32 v54, v46, v47 op_sel:[0,0,1]
	v_med3_f32 v38, v38, s22, v132
	v_med3_f32 v39, v39, s22, v132
	v_mov_b32_e32 v46, v99
	v_cvt_pk_fp8_f32 v46, v38, v39
	v_pk_mul_f32 v[40:41], v[40:41], v[154:155] op_sel_hi:[1,0]
	v_pk_mul_f32 v[30:31], v[30:31], v[154:155] op_sel_hi:[1,0]
	v_pk_fma_f32 v[38:39], v[110:111], v[40:41], v[76:77]
	v_pk_fma_f32 v[30:31], v[108:109], v[30:31], v[70:71]
	v_med3_f32 v38, v38, s22, v132
	v_med3_f32 v39, v39, s22, v132
	v_cvt_pk_fp8_f32 v46, v38, v39 op_sel:[0,0,1]
	v_med3_f32 v30, v30, s22, v132
	v_med3_f32 v31, v31, s22, v132
	v_mov_b32_e32 v38, v99
	v_cvt_pk_fp8_f32 v38, v30, v31
	v_pk_mul_f32 v[32:33], v[32:33], v[154:155] op_sel_hi:[1,0]
	v_pk_mul_f32 v[22:23], v[22:23], v[154:155] op_sel_hi:[1,0]
	v_pk_fma_f32 v[30:31], v[106:107], v[32:33], v[72:73]
	v_pk_fma_f32 v[22:23], v[152:153], v[22:23], v[66:67]
	v_med3_f32 v30, v30, s22, v132
	v_med3_f32 v31, v31, s22, v132
	v_cvt_pk_fp8_f32 v38, v30, v31 op_sel:[0,0,1]
	v_med3_f32 v22, v22, s22, v132
	v_med3_f32 v23, v23, s22, v132
	v_mov_b32_e32 v30, v99
	v_cvt_pk_fp8_f32 v30, v22, v23
	v_pk_mul_f32 v[24:25], v[24:25], v[154:155] op_sel_hi:[1,0]
	v_pk_mul_f32 v[14:15], v[14:15], v[154:155] op_sel_hi:[1,0]
	v_pk_fma_f32 v[22:23], v[92:93], v[24:25], v[68:69]
	s_waitcnt vmcnt(1)
	v_pk_fma_f32 v[14:15], v[140:141], v[14:15], v[144:145]
	v_med3_f32 v22, v22, s22, v132
	v_med3_f32 v23, v23, s22, v132
	v_cvt_pk_fp8_f32 v30, v22, v23 op_sel:[0,0,1]
	v_med3_f32 v14, v14, s22, v132
	v_med3_f32 v15, v15, s22, v132
	v_mov_b32_e32 v22, v99
	v_cvt_pk_fp8_f32 v22, v14, v15
	v_pk_mul_f32 v[16:17], v[16:17], v[154:155] op_sel_hi:[1,0]
	v_pk_mul_f32 v[6:7], v[6:7], v[154:155] op_sel_hi:[1,0]
	v_pk_fma_f32 v[14:15], v[142:143], v[16:17], v[146:147]
	s_waitcnt vmcnt(0)
	v_pk_fma_f32 v[6:7], v[148:149], v[6:7], v[94:95]
	v_med3_f32 v14, v14, s22, v132
	v_med3_f32 v15, v15, s22, v132
	v_cvt_pk_fp8_f32 v22, v14, v15 op_sel:[0,0,1]
	v_med3_f32 v6, v6, s22, v132
	v_med3_f32 v7, v7, s22, v132
	v_mov_b32_e32 v14, v99
	v_cvt_pk_fp8_f32 v14, v6, v7
	v_pk_mul_f32 v[8:9], v[8:9], v[154:155] op_sel_hi:[1,0]
	global_store_dword v[156:157], v86, off
	global_store_dword v[156:157], v62, off offset:256
	global_store_dword v[156:157], v54, off offset:512
	global_store_dword v[156:157], v46, off offset:768
	v_pk_fma_f32 v[6:7], v[150:151], v[8:9], v[96:97]
	s_nop 0
	v_med3_f32 v6, v6, s22, v132
	v_med3_f32 v7, v7, s22, v132
	v_cvt_pk_fp8_f32 v14, v6, v7 op_sel:[0,0,1]
	global_store_dword v[156:157], v38, off offset:1024
	global_store_dword v[156:157], v30, off offset:1280
	global_store_dword v[156:157], v22, off offset:1536
	global_store_dword v[156:157], v14, off offset:1792
	global_load_dwordx4 v[66:69], v98, s[16:17]
	global_load_dwordx4 v[70:73], v98, s[6:7]
	global_load_dwordx4 v[74:77], v1, s[16:17]
	global_load_dwordx4 v[78:81], v98, s[6:7] offset:1024
	global_load_dwordx4 v[82:85], v129, s[16:17]
	global_load_dwordx4 v[86:89], v98, s[6:7] offset:2048
	global_load_dwordx4 v[92:95], v130, s[16:17]
	global_load_dwordx4 v[106:109], v98, s[6:7] offset:3072
	global_load_dwordx4 v[110:113], v126, s[16:17]
	global_load_dwordx4 v[114:117], v126, s[6:7]
	global_load_dwordx4 v[118:121], v127, s[16:17]
	global_load_dwordx4 v[122:125], v127, s[6:7]
	global_load_dwordx4 v[140:143], v131, s[16:17]
	global_load_dwordx4 v[144:147], v131, s[6:7]
	global_load_dwordx4 v[148:151], v128, s[16:17]
	global_load_dwordx4 v[152:155], v128, s[6:7]
	global_load_dwordx4 v[156:159], v98, s[12:13]
	global_load_dwordx4 v[160:163], v98, s[12:13] offset:1024
	v_lshl_add_u64 v[6:7], v[102:103], 0, s[14:15]
	global_load_dwordx4 v[62:65], v[6:7], off nt
	global_load_dwordx4 v[54:57], v[6:7], off offset:1024 nt
	global_load_dwordx4 v[164:167], v98, s[12:13] offset:2048
	global_load_dwordx4 v[46:49], v[6:7], off offset:2048 nt
	global_load_dwordx4 v[38:41], v[6:7], off offset:3072 nt
	v_add_co_u32_e32 v6, vcc, s24, v6
	s_waitcnt vmcnt(22)
	v_pk_add_f32 v[66:67], v[66:67], 1.0 op_sel_hi:[1,0]
	v_addc_co_u32_e32 v7, vcc, 0, v7, vcc
	global_load_dwordx4 v[30:33], v[6:7], off nt
	global_load_dwordx4 v[22:25], v[6:7], off offset:1024 nt
	global_load_dwordx4 v[14:17], v[6:7], off offset:2048 nt
	s_nop 0
	global_load_dwordx4 v[6:9], v[6:7], off offset:3072 nt
	v_pk_add_f32 v[68:69], v[68:69], 1.0 op_sel_hi:[1,0]
	global_load_dwordx4 v[168:171], v98, s[12:13] offset:3072
	s_waitcnt vmcnt(26)
	v_pk_mul_f32 v[172:173], v[70:71], v[66:67]
	s_waitcnt vmcnt(25)
	v_pk_add_f32 v[66:67], v[76:77], 1.0 op_sel_hi:[1,0]
	v_pk_mul_f32 v[96:97], v[72:73], v[68:69]
	v_pk_add_f32 v[68:69], v[74:75], 1.0 op_sel_hi:[1,0]
	s_waitcnt vmcnt(24)
	v_pk_mul_f32 v[174:175], v[80:81], v[66:67]
	s_waitcnt vmcnt(23)
	v_pk_add_f32 v[66:67], v[84:85], 1.0 op_sel_hi:[1,0]
	v_pk_mul_f32 v[176:177], v[78:79], v[68:69]
	v_pk_add_f32 v[68:69], v[82:83], 1.0 op_sel_hi:[1,0]
	s_waitcnt vmcnt(22)
	v_pk_mul_f32 v[82:83], v[88:89], v[66:67]
	s_waitcnt vmcnt(21)
	v_pk_add_f32 v[66:67], v[94:95], 1.0 op_sel_hi:[1,0]
	v_pk_mul_f32 v[84:85], v[86:87], v[68:69]
	s_waitcnt vmcnt(20)
	v_pk_mul_f32 v[86:87], v[108:109], v[66:67]
	global_load_dwordx4 v[66:69], v126, s[12:13]
	v_pk_add_f32 v[70:71], v[92:93], 1.0 op_sel_hi:[1,0]
	s_waitcnt vmcnt(20)
	v_pk_add_f32 v[72:73], v[110:111], 1.0 op_sel_hi:[1,0]
	v_pk_mul_f32 v[88:89], v[106:107], v[70:71]
	v_pk_add_f32 v[70:71], v[112:113], 1.0 op_sel_hi:[1,0]
	s_waitcnt vmcnt(19)
	v_pk_mul_f32 v[94:95], v[114:115], v[72:73]
	v_pk_mul_f32 v[92:93], v[116:117], v[70:71]
	global_load_dwordx4 v[70:73], v127, s[12:13]
	s_waitcnt vmcnt(19)
	v_pk_add_f32 v[74:75], v[120:121], 1.0 op_sel_hi:[1,0]
	v_pk_add_f32 v[76:77], v[118:119], 1.0 op_sel_hi:[1,0]
	s_waitcnt vmcnt(18)
	v_pk_mul_f32 v[106:107], v[124:125], v[74:75]
	v_pk_mul_f32 v[108:109], v[122:123], v[76:77]
	global_load_dwordx4 v[74:77], v131, s[12:13]
	s_waitcnt vmcnt(18)
	v_pk_add_f32 v[78:79], v[142:143], 1.0 op_sel_hi:[1,0]
	v_cmp_gt_f32_e32 vcc, s23, v90
	s_waitcnt vmcnt(17)
	v_pk_mul_f32 v[110:111], v[146:147], v[78:79]
	v_mul_f32_e32 v78, 0x4b800000, v90
	v_pk_add_f32 v[80:81], v[140:141], 1.0 op_sel_hi:[1,0]
	v_cndmask_b32_e32 v78, v90, v78, vcc
	v_pk_mul_f32 v[112:113], v[144:145], v[80:81]
	v_rsq_f32_e32 v118, v78
	global_load_dwordx4 v[78:81], v128, s[12:13]
	s_waitcnt vmcnt(17)
	v_pk_add_f32 v[114:115], v[150:151], 1.0 op_sel_hi:[1,0]
	v_pk_add_f32 v[116:117], v[148:149], 1.0 op_sel_hi:[1,0]
	s_waitcnt vmcnt(16)
	v_pk_mul_f32 v[90:91], v[154:155], v[114:115]
	v_pk_mul_f32 v[114:115], v[152:153], v[116:117]
	v_mul_f32_e32 v116, 0x45800000, v118
	v_cndmask_b32_e32 v116, v118, v116, vcc
	v_pk_mul_f32 v[58:59], v[58:59], v[116:117] op_sel_hi:[1,0]
	v_pk_mul_f32 v[60:61], v[60:61], v[116:117] op_sel_hi:[1,0]
	s_waitcnt vmcnt(15)
	v_pk_fma_f32 v[58:59], v[172:173], v[58:59], v[156:157]
	v_mov_b32_e32 v117, v99
	v_med3_f32 v58, v58, s22, v132
	v_med3_f32 v59, v59, s22, v132
	v_cvt_pk_fp8_f32 v117, v58, v59
	v_pk_fma_f32 v[58:59], v[96:97], v[60:61], v[158:159]
	s_lshl_b64 s[12:13], s[10:11], 11
	v_med3_f32 v58, v58, s22, v132
	v_med3_f32 v59, v59, s22, v132
	v_cvt_pk_fp8_f32 v117, v58, v59 op_sel:[0,0,1]
	v_mov_b32_e32 v58, v99
	v_lshl_add_u64 v[118:119], v[100:101], 0, s[12:13]
	s_addk_i32 s10, 0x1000
	v_pk_mul_f32 v[50:51], v[50:51], v[116:117] op_sel_hi:[1,0]
	v_pk_mul_f32 v[52:53], v[52:53], v[116:117] op_sel_hi:[1,0]
	s_waitcnt vmcnt(14)
	v_pk_fma_f32 v[50:51], v[176:177], v[50:51], v[160:161]
	v_pk_mul_f32 v[42:43], v[42:43], v[116:117] op_sel_hi:[1,0]
	v_med3_f32 v50, v50, s22, v132
	v_med3_f32 v51, v51, s22, v132
	v_cvt_pk_fp8_f32 v58, v50, v51
	v_pk_fma_f32 v[50:51], v[174:175], v[52:53], v[162:163]
	s_waitcnt vmcnt(11)
	v_pk_fma_f32 v[42:43], v[84:85], v[42:43], v[164:165]
	v_med3_f32 v50, v50, s22, v132
	v_med3_f32 v51, v51, s22, v132
	v_cvt_pk_fp8_f32 v58, v50, v51 op_sel:[0,0,1]
	v_med3_f32 v42, v42, s22, v132
	v_med3_f32 v43, v43, s22, v132
	v_mov_b32_e32 v50, v99
	v_cvt_pk_fp8_f32 v50, v42, v43
	v_pk_mul_f32 v[44:45], v[44:45], v[116:117] op_sel_hi:[1,0]
	v_pk_mul_f32 v[34:35], v[34:35], v[116:117] op_sel_hi:[1,0]
	v_pk_fma_f32 v[42:43], v[82:83], v[44:45], v[166:167]
	v_pk_mul_f32 v[36:37], v[36:37], v[116:117] op_sel_hi:[1,0]
	v_med3_f32 v42, v42, s22, v132
	v_med3_f32 v43, v43, s22, v132
	v_cvt_pk_fp8_f32 v50, v42, v43 op_sel:[0,0,1]
	v_mov_b32_e32 v42, v99
	s_waitcnt vmcnt(4)
	v_pk_fma_f32 v[34:35], v[88:89], v[34:35], v[168:169]
	v_pk_mul_f32 v[26:27], v[26:27], v[116:117] op_sel_hi:[1,0]
	v_med3_f32 v34, v34, s22, v132
	v_med3_f32 v35, v35, s22, v132
	v_cvt_pk_fp8_f32 v42, v34, v35
	v_pk_fma_f32 v[34:35], v[86:87], v[36:37], v[170:171]
	v_pk_mul_f32 v[28:29], v[28:29], v[116:117] op_sel_hi:[1,0]
	v_med3_f32 v34, v34, s22, v132
	v_med3_f32 v35, v35, s22, v132
	v_cvt_pk_fp8_f32 v42, v34, v35 op_sel:[0,0,1]
	v_mov_b32_e32 v34, v99
	v_pk_mul_f32 v[18:19], v[18:19], v[116:117] op_sel_hi:[1,0]
	v_pk_mul_f32 v[20:21], v[20:21], v[116:117] op_sel_hi:[1,0]
	s_waitcnt vmcnt(3)
	v_pk_fma_f32 v[26:27], v[94:95], v[26:27], v[66:67]
	v_pk_mul_f32 v[10:11], v[10:11], v[116:117] op_sel_hi:[1,0]
	v_med3_f32 v26, v26, s22, v132
	v_med3_f32 v27, v27, s22, v132
	v_cvt_pk_fp8_f32 v34, v26, v27
	v_pk_fma_f32 v[26:27], v[92:93], v[28:29], v[68:69]
	v_pk_mul_f32 v[12:13], v[12:13], v[116:117] op_sel_hi:[1,0]
	v_med3_f32 v26, v26, s22, v132
	v_med3_f32 v27, v27, s22, v132
	s_waitcnt vmcnt(2)
	v_pk_fma_f32 v[18:19], v[108:109], v[18:19], v[70:71]
	v_cvt_pk_fp8_f32 v34, v26, v27 op_sel:[0,0,1]
	v_med3_f32 v18, v18, s22, v132
	v_med3_f32 v19, v19, s22, v132
	v_mov_b32_e32 v26, v99
	v_cvt_pk_fp8_f32 v26, v18, v19
	v_pk_fma_f32 v[18:19], v[106:107], v[20:21], v[72:73]
	s_waitcnt vmcnt(1)
	v_pk_fma_f32 v[10:11], v[112:113], v[10:11], v[74:75]
	v_med3_f32 v18, v18, s22, v132
	v_med3_f32 v19, v19, s22, v132
	v_cvt_pk_fp8_f32 v26, v18, v19 op_sel:[0,0,1]
	v_med3_f32 v10, v10, s22, v132
	v_med3_f32 v11, v11, s22, v132
	v_mov_b32_e32 v18, v99
	v_cvt_pk_fp8_f32 v18, v10, v11
	v_pk_fma_f32 v[10:11], v[110:111], v[12:13], v[76:77]
	v_pk_mul_f32 v[2:3], v[2:3], v[116:117] op_sel_hi:[1,0]
	v_med3_f32 v10, v10, s22, v132
	v_med3_f32 v11, v11, s22, v132
	s_waitcnt vmcnt(0)
	v_pk_fma_f32 v[2:3], v[114:115], v[2:3], v[78:79]
	v_cvt_pk_fp8_f32 v18, v10, v11 op_sel:[0,0,1]
	v_med3_f32 v2, v2, s22, v132
	v_med3_f32 v3, v3, s22, v132
	v_mov_b32_e32 v10, v99
	s_mul_i32 s12, s9, 0x3000
	v_cvt_pk_fp8_f32 v10, v2, v3
	s_ashr_i32 s11, s10, 31
	s_ashr_i32 s13, s12, 31
	v_pk_mul_f32 v[4:5], v[4:5], v[116:117] op_sel_hi:[1,0]
	s_lshl_b64 s[16:17], s[10:11], 13
	s_lshl_b64 s[12:13], s[12:13], 2
	v_pk_fma_f32 v[2:3], v[90:91], v[4:5], v[80:81]
	s_add_u32 s12, s3, s12
	v_med3_f32 v2, v2, s22, v132
	v_med3_f32 v3, v3, s22, v132
	s_addc_u32 s13, s2, s13
	v_cvt_pk_fp8_f32 v10, v2, v3 op_sel:[0,0,1]
	s_add_u32 s14, s12, 0x2000
	global_store_dword v[118:119], v117, off
	global_store_dword v[118:119], v58, off offset:256
	global_store_dword v[118:119], v50, off offset:512
	global_store_dword v[118:119], v42, off offset:768
	global_store_dword v[118:119], v34, off offset:1024
	global_store_dword v[118:119], v26, off offset:1280
	global_store_dword v[118:119], v18, off offset:1536
	global_store_dword v[118:119], v10, off offset:1792
	s_addc_u32 s15, s13, 0
	global_load_dwordx4 v[66:69], v98, s[14:15]
	global_load_dwordx4 v[70:73], v98, s[6:7]
	global_load_dwordx4 v[74:77], v1, s[14:15]
	global_load_dwordx4 v[78:81], v98, s[6:7] offset:1024
	global_load_dwordx4 v[112:115], v129, s[14:15]
	global_load_dwordx4 v[116:119], v98, s[6:7] offset:2048
	global_load_dwordx4 v[120:123], v130, s[14:15]
	global_load_dwordx4 v[140:143], v98, s[6:7] offset:3072
	global_load_dwordx4 v[144:147], v126, s[14:15]
	v_lshl_add_u64 v[2:3], v[102:103], 0, s[16:17]
	global_load_dwordx4 v[58:61], v[2:3], off nt
	global_load_dwordx4 v[50:53], v[2:3], off offset:1024 nt
	global_load_dwordx4 v[42:45], v[2:3], off offset:2048 nt
	global_load_dwordx4 v[34:37], v[2:3], off offset:3072 nt
	v_add_co_u32_e32 v82, vcc, s24, v2
	v_mov_b32_e32 v156, v63
	s_nop 0
	v_addc_co_u32_e32 v83, vcc, 0, v3, vcc
	global_load_dwordx4 v[26:29], v[82:83], off nt
	global_load_dwordx4 v[18:21], v[82:83], off offset:1024 nt
	global_load_dwordx4 v[10:13], v[82:83], off offset:2048 nt
	global_load_dwordx4 v[2:5], v[82:83], off offset:3072 nt
	global_load_dwordx4 v[86:89], v128, s[14:15]
	v_mov_b32_e32 v157, v55
	v_mov_b32_e32 v154, v62
	v_mov_b32_e32 v155, v54
	v_pk_mul_f32 v[156:157], v[156:157], v[156:157]
	v_mov_b32_e32 v158, v65
	v_mov_b32_e32 v159, v57
	v_pk_fma_f32 v[154:155], v[154:155], v[154:155], v[156:157]
	v_mov_b32_e32 v156, v64
	v_mov_b32_e32 v157, v56
	v_pk_mul_f32 v[158:159], v[158:159], v[158:159]
	v_mul_f32_e32 v139, v30, v30
	v_pk_fma_f32 v[156:157], v[156:157], v[156:157], v[158:159]
	v_pk_mul_f32 v[158:159], v[46:47], v[46:47]
	v_pk_add_f32 v[154:155], v[154:155], v[156:157]
	v_pk_mul_f32 v[156:157], v[48:49], v[48:49]
	v_pk_add_f32 v[154:155], v[154:155], v[154:155] op_sel:[0,1] op_sel_hi:[1,0]
	v_pk_mov_b32 v[160:161], v[158:159], v[156:157] op_sel:[1,0]
	v_mov_b32_e32 v159, v157
	v_pk_add_f32 v[156:157], v[160:161], v[158:159]
	v_mul_f32_e32 v158, v31, v31
	v_pk_add_f32 v[156:157], v[156:157], v[156:157] op_sel:[0,1] op_sel_hi:[1,0]
	v_mov_b32_e32 v155, v139
	v_mov_b32_e32 v157, v158
	v_pk_add_f32 v[154:155], v[154:155], v[156:157]
	v_mul_f32_e32 v156, v39, v39
	v_mul_f32_e32 v159, v32, v32
	v_pk_fma_f32 v[156:157], v[38:39], v[38:39], v[156:157] op_sel_hi:[1,1,0]
	v_mul_f32_e32 v158, v41, v41
	v_mul_f32_e32 v160, v33, v33
	v_mov_b32_e32 v157, v159
	v_pk_fma_f32 v[158:159], v[40:41], v[40:41], v[158:159] op_sel_hi:[1,1,0]
	v_mul_f32_e32 v139, v6, v6
	v_mov_b32_e32 v159, v160
	v_pk_add_f32 v[156:157], v[156:157], v[158:159]
	v_pk_mul_f32 v[158:159], v[22:23], v[22:23]
	v_pk_add_f32 v[154:155], v[154:155], v[156:157]
	v_pk_mul_f32 v[156:157], v[24:25], v[24:25]
	v_pk_add_f32 v[154:155], v[154:155], v[154:155] op_sel:[0,1] op_sel_hi:[1,0]
	v_pk_mov_b32 v[160:161], v[158:159], v[156:157] op_sel:[1,0]
	v_mov_b32_e32 v159, v157
	v_pk_add_f32 v[156:157], v[160:161], v[158:159]
	v_mul_f32_e32 v158, v7, v7
	v_pk_add_f32 v[156:157], v[156:157], v[156:157] op_sel:[0,1] op_sel_hi:[1,0]
	v_mov_b32_e32 v155, v139
	v_mov_b32_e32 v157, v158
	v_pk_add_f32 v[154:155], v[154:155], v[156:157]
	v_mul_f32_e32 v156, v15, v15
	v_mul_f32_e32 v159, v8, v8
	v_pk_fma_f32 v[156:157], v[14:15], v[14:15], v[156:157] op_sel_hi:[1,1,0]
	v_mul_f32_e32 v158, v17, v17
	v_mul_f32_e32 v160, v9, v9
	v_mov_b32_e32 v157, v159
	v_pk_fma_f32 v[158:159], v[16:17], v[16:17], v[158:159] op_sel_hi:[1,1,0]
	s_lshl_b64 s[0:1], s[0:1], 11
	v_mov_b32_e32 v159, v160
	v_pk_add_f32 v[156:157], v[156:157], v[158:159]
	s_waitcnt vmcnt(17)
	v_pk_add_f32 v[68:69], v[68:69], 1.0 op_sel_hi:[1,0]
	v_pk_add_f32 v[66:67], v[66:67], 1.0 op_sel_hi:[1,0]
	s_waitcnt vmcnt(16)
	v_pk_mul_f32 v[92:93], v[72:73], v[68:69]
	v_pk_mul_f32 v[96:97], v[70:71], v[66:67]
	s_waitcnt vmcnt(15)
	v_pk_add_f32 v[66:67], v[76:77], 1.0 op_sel_hi:[1,0]
	v_pk_add_f32 v[68:69], v[74:75], 1.0 op_sel_hi:[1,0]
	s_waitcnt vmcnt(14)
	v_pk_mul_f32 v[108:109], v[80:81], v[66:67]
	v_pk_mul_f32 v[110:111], v[78:79], v[68:69]
	s_waitcnt vmcnt(13)
	v_pk_add_f32 v[66:67], v[114:115], 1.0 op_sel_hi:[1,0]
	v_pk_add_f32 v[68:69], v[112:113], 1.0 op_sel_hi:[1,0]
	s_waitcnt vmcnt(12)
	v_pk_mul_f32 v[102:103], v[118:119], v[66:67]
	v_pk_mul_f32 v[106:107], v[116:117], v[68:69]
	s_waitcnt vmcnt(11)
	v_pk_add_f32 v[66:67], v[122:123], 1.0 op_sel_hi:[1,0]
	v_pk_add_f32 v[68:69], v[120:121], 1.0 op_sel_hi:[1,0]
	global_load_dwordx4 v[82:85], v98, s[12:13]
	global_load_dwordx4 v[78:81], v98, s[12:13] offset:1024
	s_waitcnt vmcnt(12)
	v_pk_mul_f32 v[90:91], v[142:143], v[66:67]
	v_pk_mul_f32 v[94:95], v[140:141], v[68:69]
	global_load_dwordx4 v[74:77], v98, s[12:13] offset:2048
	global_load_dwordx4 v[70:73], v98, s[12:13] offset:3072
	s_waitcnt vmcnt(13)
	v_pk_add_f32 v[124:125], v[146:147], 1.0 op_sel_hi:[1,0]
	v_pk_add_f32 v[152:153], v[144:145], 1.0 op_sel_hi:[1,0]
	global_load_dwordx4 v[112:115], v126, s[6:7]
	global_load_dwordx4 v[66:69], v126, s[12:13]
	global_load_dwordx4 v[116:119], v127, s[6:7]
	global_load_dwordx4 v[120:123], v127, s[14:15]
	global_load_dwordx4 v[140:143], v131, s[6:7]
	global_load_dwordx4 v[144:147], v131, s[14:15]
	global_load_dwordx4 v[148:151], v128, s[6:7]
	s_waitcnt vmcnt(19)
	v_mov_b32_e32 v158, v59
	s_waitcnt vmcnt(18)
	v_mov_b32_e32 v159, v51
	v_pk_add_f32 v[154:155], v[154:155], v[156:157]
	v_mov_b32_e32 v156, v58
	v_mov_b32_e32 v157, v50
	v_pk_mul_f32 v[158:159], v[158:159], v[158:159]
	v_mov_b32_e32 v160, v61
	v_mov_b32_e32 v161, v53
	v_pk_fma_f32 v[156:157], v[156:157], v[156:157], v[158:159]
	v_mov_b32_e32 v158, v60
	v_mov_b32_e32 v159, v52
	v_pk_mul_f32 v[160:161], v[160:161], v[160:161]
	s_waitcnt vmcnt(15)
	v_mul_f32_e32 v139, v26, v26
	v_pk_fma_f32 v[158:159], v[158:159], v[158:159], v[160:161]
	v_pk_mul_f32 v[160:161], v[42:43], v[42:43]
	v_pk_add_f32 v[156:157], v[156:157], v[158:159]
	v_pk_mul_f32 v[158:159], v[44:45], v[44:45]
	v_pk_add_f32 v[156:157], v[156:157], v[156:157] op_sel:[0,1] op_sel_hi:[1,0]
	v_pk_mov_b32 v[162:163], v[160:161], v[158:159] op_sel:[1,0]
	v_mov_b32_e32 v161, v159
	v_pk_add_f32 v[158:159], v[162:163], v[160:161]
	v_mul_f32_e32 v160, v27, v27
	v_pk_add_f32 v[158:159], v[158:159], v[158:159] op_sel:[0,1] op_sel_hi:[1,0]
	v_mov_b32_e32 v157, v139
	v_mov_b32_e32 v159, v160
	v_pk_add_f32 v[156:157], v[156:157], v[158:159]
	v_mul_f32_e32 v158, v35, v35
	v_mul_f32_e32 v161, v28, v28
	v_pk_fma_f32 v[158:159], v[34:35], v[34:35], v[158:159] op_sel_hi:[1,1,0]
	v_mul_f32_e32 v160, v37, v37
	v_mul_f32_e32 v162, v29, v29
	v_mov_b32_e32 v159, v161
	v_pk_fma_f32 v[160:161], v[36:37], v[36:37], v[160:161] op_sel_hi:[1,1,0]
	s_waitcnt vmcnt(12)
	v_mul_f32_e32 v139, v2, v2
	v_mov_b32_e32 v161, v162
	v_pk_add_f32 v[158:159], v[158:159], v[160:161]
	v_pk_mul_f32 v[160:161], v[18:19], v[18:19]
	v_pk_add_f32 v[156:157], v[156:157], v[158:159]
	v_pk_mul_f32 v[158:159], v[20:21], v[20:21]
	v_pk_add_f32 v[156:157], v[156:157], v[156:157] op_sel:[0,1] op_sel_hi:[1,0]
	v_pk_mov_b32 v[162:163], v[160:161], v[158:159] op_sel:[1,0]
	v_mov_b32_e32 v161, v159
	v_pk_add_f32 v[158:159], v[162:163], v[160:161]
	v_mul_f32_e32 v160, v3, v3
	v_pk_add_f32 v[158:159], v[158:159], v[158:159] op_sel:[0,1] op_sel_hi:[1,0]
	v_mov_b32_e32 v157, v139
	v_mov_b32_e32 v159, v160
	v_pk_add_f32 v[156:157], v[156:157], v[158:159]
	v_mul_f32_e32 v158, v11, v11
	v_mul_f32_e32 v161, v4, v4
	v_pk_fma_f32 v[158:159], v[10:11], v[10:11], v[158:159] op_sel_hi:[1,1,0]
	v_mul_f32_e32 v160, v13, v13
	v_mul_f32_e32 v162, v5, v5
	v_mov_b32_e32 v159, v161
	v_pk_fma_f32 v[160:161], v[12:13], v[12:13], v[160:161] op_sel_hi:[1,1,0]
	s_waitcnt vmcnt(11)
	v_pk_add_f32 v[86:87], v[86:87], 1.0 op_sel_hi:[1,0]
	v_mov_b32_e32 v161, v162
	v_pk_add_f32 v[158:159], v[158:159], v[160:161]
	v_pk_add_f32 v[88:89], v[88:89], 1.0 op_sel_hi:[1,0]
	v_pk_add_f32 v[156:157], v[156:157], v[158:159]
	v_mov_b32_e32 v159, v154
	v_mov_b32_e32 v158, v156
	v_mov_b32_e32 v154, v157
	v_pk_add_f32 v[154:155], v[158:159], v[154:155]
	ds_bpermute_b32 v139, v138, v155
	ds_bpermute_b32 v138, v138, v154
	s_waitcnt lgkmcnt(0)
	v_pk_add_f32 v[138:139], v[154:155], v[138:139]
	ds_bpermute_b32 v155, v137, v139
	ds_bpermute_b32 v154, v137, v138
	s_waitcnt vmcnt(6)
	v_pk_mul_f32 v[124:125], v[114:115], v[124:125]
	v_pk_mul_f32 v[152:153], v[112:113], v[152:153]
	global_load_dwordx4 v[112:115], v127, s[12:13]
	s_waitcnt vmcnt(4)
	v_pk_add_f32 v[122:123], v[122:123], 1.0 op_sel_hi:[1,0]
	v_pk_add_f32 v[120:121], v[120:121], 1.0 op_sel_hi:[1,0]
	v_pk_mul_f32 v[156:157], v[118:119], v[122:123]
	s_waitcnt lgkmcnt(0)
	v_pk_add_f32 v[122:123], v[138:139], v[154:155]
	v_pk_mul_f32 v[158:159], v[116:117], v[120:121]
	ds_bpermute_b32 v137, v136, v123
	ds_bpermute_b32 v136, v136, v122
	global_load_dwordx4 v[116:119], v131, s[12:13]
	s_waitcnt vmcnt(3)
	v_pk_add_f32 v[120:121], v[146:147], 1.0 op_sel_hi:[1,0]
	v_pk_add_f32 v[138:139], v[144:145], 1.0 op_sel_hi:[1,0]
	v_pk_mul_f32 v[142:143], v[142:143], v[120:121]
	s_waitcnt lgkmcnt(0)
	v_pk_add_f32 v[136:137], v[122:123], v[136:137]
	global_load_dwordx4 v[120:123], v128, s[12:13]
	v_pk_mul_f32 v[138:139], v[140:141], v[138:139]
	ds_bpermute_b32 v141, v135, v137
	ds_bpermute_b32 v140, v135, v136
	v_lshl_add_u64 v[144:145], v[100:101], 0, s[0:1]
	s_lshr_b32 s0, s10, 11
	s_mulk_i32 s0, 0x3000
	s_ashr_i32 s1, s0, 31
	s_waitcnt lgkmcnt(0)
	v_pk_add_f32 v[136:137], v[136:137], v[140:141]
	ds_bpermute_b32 v135, v134, v137
	ds_bpermute_b32 v134, v134, v136
	s_waitcnt vmcnt(3)
	v_pk_mul_f32 v[140:141], v[148:149], v[86:87]
	v_pk_mul_f32 v[88:89], v[150:151], v[88:89]
	s_lshl_b64 s[0:1], s[0:1], 2
	s_add_u32 s0, s3, s0
	s_waitcnt lgkmcnt(0)
	v_pk_add_f32 v[86:87], v[136:137], v[134:135]
	ds_bpermute_b32 v135, v133, v87
	ds_bpermute_b32 v134, v133, v86
	s_addc_u32 s1, s2, s1
	s_waitcnt lgkmcnt(0)
	v_pk_add_f32 v[86:87], v[86:87], v[134:135]
	s_nop 0
	v_pk_fma_f32 v[86:87], v[86:87], s[8:9], v[104:105] op_sel_hi:[1,0,0]
	s_add_u32 s8, s0, 0x2000
	v_mul_f32_e32 v104, 0x4b800000, v87
	v_cmp_gt_f32_e32 vcc, s23, v87
	s_addc_u32 s9, s1, 0
	s_nop 0
	v_cndmask_b32_e32 v87, v87, v104, vcc
	v_rsq_f32_e32 v87, v87
	s_nop 0
	v_mul_f32_e32 v104, 0x45800000, v87
	v_cndmask_b32_e32 v104, v87, v104, vcc
	v_pk_mul_f32 v[62:63], v[62:63], v[104:105] op_sel_hi:[1,0]
	v_pk_mul_f32 v[64:65], v[64:65], v[104:105] op_sel_hi:[1,0]
	v_pk_fma_f32 v[62:63], v[96:97], v[62:63], v[82:83]
	v_mov_b32_e32 v82, v99
	v_med3_f32 v62, v62, s22, v132
	v_med3_f32 v63, v63, s22, v132
	v_cvt_pk_fp8_f32 v82, v62, v63
	v_pk_fma_f32 v[62:63], v[92:93], v[64:65], v[84:85]
	v_pk_mul_f32 v[54:55], v[54:55], v[104:105] op_sel_hi:[1,0]
	v_med3_f32 v62, v62, s22, v132
	v_med3_f32 v63, v63, s22, v132
	v_pk_fma_f32 v[54:55], v[110:111], v[54:55], v[78:79]
	v_cvt_pk_fp8_f32 v82, v62, v63 op_sel:[0,0,1]
	v_med3_f32 v54, v54, s22, v132
	v_med3_f32 v55, v55, s22, v132
	v_mov_b32_e32 v62, v99
	v_cvt_pk_fp8_f32 v62, v54, v55
	v_pk_mul_f32 v[56:57], v[56:57], v[104:105] op_sel_hi:[1,0]
	v_pk_mul_f32 v[46:47], v[46:47], v[104:105] op_sel_hi:[1,0]
	v_pk_fma_f32 v[54:55], v[108:109], v[56:57], v[80:81]
	v_pk_fma_f32 v[46:47], v[106:107], v[46:47], v[74:75]
	v_med3_f32 v54, v54, s22, v132
	v_med3_f32 v55, v55, s22, v132
	v_cvt_pk_fp8_f32 v62, v54, v55 op_sel:[0,0,1]
	v_med3_f32 v46, v46, s22, v132
	v_med3_f32 v47, v47, s22, v132
	v_mov_b32_e32 v54, v99
	v_cvt_pk_fp8_f32 v54, v46, v47
	v_pk_mul_f32 v[48:49], v[48:49], v[104:105] op_sel_hi:[1,0]
	v_pk_mul_f32 v[38:39], v[38:39], v[104:105] op_sel_hi:[1,0]
	v_pk_fma_f32 v[46:47], v[102:103], v[48:49], v[76:77]
	v_pk_fma_f32 v[38:39], v[94:95], v[38:39], v[70:71]
	v_med3_f32 v46, v46, s22, v132
	v_med3_f32 v47, v47, s22, v132
	v_cvt_pk_fp8_f32 v54, v46, v47 op_sel:[0,0,1]
	v_med3_f32 v38, v38, s22, v132
	v_med3_f32 v39, v39, s22, v132
	v_mov_b32_e32 v46, v99
	v_cvt_pk_fp8_f32 v46, v38, v39
	v_pk_mul_f32 v[40:41], v[40:41], v[104:105] op_sel_hi:[1,0]
	v_pk_mul_f32 v[30:31], v[30:31], v[104:105] op_sel_hi:[1,0]
	v_pk_fma_f32 v[38:39], v[90:91], v[40:41], v[72:73]
	v_pk_fma_f32 v[30:31], v[152:153], v[30:31], v[66:67]
	v_med3_f32 v38, v38, s22, v132
	v_med3_f32 v39, v39, s22, v132
	v_cvt_pk_fp8_f32 v46, v38, v39 op_sel:[0,0,1]
	v_med3_f32 v30, v30, s22, v132
	v_med3_f32 v31, v31, s22, v132
	v_mov_b32_e32 v38, v99
	v_cvt_pk_fp8_f32 v38, v30, v31
	v_pk_mul_f32 v[32:33], v[32:33], v[104:105] op_sel_hi:[1,0]
	v_pk_mul_f32 v[22:23], v[22:23], v[104:105] op_sel_hi:[1,0]
	v_pk_fma_f32 v[30:31], v[124:125], v[32:33], v[68:69]
	s_waitcnt vmcnt(2)
	v_pk_fma_f32 v[22:23], v[158:159], v[22:23], v[112:113]
	v_med3_f32 v30, v30, s22, v132
	v_med3_f32 v31, v31, s22, v132
	v_cvt_pk_fp8_f32 v38, v30, v31 op_sel:[0,0,1]
	v_med3_f32 v22, v22, s22, v132
	v_med3_f32 v23, v23, s22, v132
	v_mov_b32_e32 v30, v99
	v_cvt_pk_fp8_f32 v30, v22, v23
	v_pk_mul_f32 v[24:25], v[24:25], v[104:105] op_sel_hi:[1,0]
	v_pk_mul_f32 v[14:15], v[14:15], v[104:105] op_sel_hi:[1,0]
	v_pk_fma_f32 v[22:23], v[156:157], v[24:25], v[114:115]
	s_waitcnt vmcnt(1)
	v_pk_fma_f32 v[14:15], v[138:139], v[14:15], v[116:117]
	v_med3_f32 v22, v22, s22, v132
	v_med3_f32 v23, v23, s22, v132
	v_cvt_pk_fp8_f32 v30, v22, v23 op_sel:[0,0,1]
	v_med3_f32 v14, v14, s22, v132
	v_med3_f32 v15, v15, s22, v132
	v_mov_b32_e32 v22, v99
	v_cvt_pk_fp8_f32 v22, v14, v15
	v_pk_mul_f32 v[16:17], v[16:17], v[104:105] op_sel_hi:[1,0]
	v_pk_mul_f32 v[6:7], v[6:7], v[104:105] op_sel_hi:[1,0]
	v_pk_fma_f32 v[14:15], v[142:143], v[16:17], v[118:119]
	s_waitcnt vmcnt(0)
	v_pk_fma_f32 v[6:7], v[140:141], v[6:7], v[120:121]
	v_med3_f32 v14, v14, s22, v132
	v_med3_f32 v15, v15, s22, v132
	v_cvt_pk_fp8_f32 v22, v14, v15 op_sel:[0,0,1]
	v_med3_f32 v6, v6, s22, v132
	v_med3_f32 v7, v7, s22, v132
	v_mov_b32_e32 v14, v99
	v_cvt_pk_fp8_f32 v14, v6, v7
	v_pk_mul_f32 v[8:9], v[8:9], v[104:105] op_sel_hi:[1,0]
	global_store_dword v[144:145], v82, off
	global_store_dword v[144:145], v62, off offset:256
	global_store_dword v[144:145], v54, off offset:512
	global_store_dword v[144:145], v46, off offset:768
	v_pk_fma_f32 v[6:7], v[88:89], v[8:9], v[122:123]
	v_cmp_gt_f32_e32 vcc, s23, v86
	v_med3_f32 v6, v6, s22, v132
	v_med3_f32 v7, v7, s22, v132
	v_cvt_pk_fp8_f32 v14, v6, v7 op_sel:[0,0,1]
	global_store_dword v[144:145], v38, off offset:1024
	global_store_dword v[144:145], v30, off offset:1280
	global_store_dword v[144:145], v22, off offset:1536
	global_store_dword v[144:145], v14, off offset:1792
	global_load_dwordx4 v[6:9], v98, s[8:9]
	s_nop 0
	global_load_dwordx4 v[14:17], v98, s[6:7]
	global_load_dwordx4 v[22:25], v1, s[8:9]
	global_load_dwordx4 v[30:33], v98, s[6:7] offset:1024
	global_load_dwordx4 v[38:41], v129, s[8:9]
	global_load_dwordx4 v[46:49], v98, s[6:7] offset:2048
	global_load_dwordx4 v[54:57], v130, s[8:9]
	global_load_dwordx4 v[62:65], v98, s[6:7] offset:3072
	global_load_dwordx4 v[66:69], v126, s[8:9]
	global_load_dwordx4 v[70:73], v126, s[6:7]
	global_load_dwordx4 v[74:77], v127, s[8:9]
	global_load_dwordx4 v[78:81], v127, s[6:7]
	global_load_dwordx4 v[82:85], v131, s[8:9]
	global_load_dwordx4 v[88:91], v131, s[6:7]
	global_load_dwordx4 v[92:95], v128, s[8:9]
	global_load_dwordx4 v[102:105], v128, s[6:7]
	global_load_dwordx4 v[106:109], v98, s[0:1]
	global_load_dwordx4 v[110:113], v98, s[0:1] offset:1024
	global_load_dwordx4 v[114:117], v98, s[0:1] offset:2048
	global_load_dwordx4 v[118:121], v98, s[0:1] offset:3072
	v_mul_f32_e32 v1, 0x4b800000, v86
	v_cndmask_b32_e32 v1, v86, v1, vcc
	v_rsq_f32_e32 v1, v1
	s_waitcnt vmcnt(19)
	v_pk_add_f32 v[8:9], v[8:9], 1.0 op_sel_hi:[1,0]
	v_pk_add_f32 v[6:7], v[6:7], 1.0 op_sel_hi:[1,0]
	s_waitcnt vmcnt(18)
	v_pk_mul_f32 v[96:97], v[16:17], v[8:9]
	v_pk_mul_f32 v[122:123], v[14:15], v[6:7]
	s_waitcnt vmcnt(17)
	v_pk_add_f32 v[6:7], v[24:25], 1.0 op_sel_hi:[1,0]
	v_pk_add_f32 v[8:9], v[22:23], 1.0 op_sel_hi:[1,0]
	s_waitcnt vmcnt(16)
	v_pk_mul_f32 v[124:125], v[32:33], v[6:7]
	v_pk_mul_f32 v[134:135], v[30:31], v[8:9]
	s_waitcnt vmcnt(15)
	v_pk_add_f32 v[6:7], v[40:41], 1.0 op_sel_hi:[1,0]
	v_pk_add_f32 v[8:9], v[38:39], 1.0 op_sel_hi:[1,0]
	s_waitcnt vmcnt(14)
	v_pk_mul_f32 v[38:39], v[48:49], v[6:7]
	v_pk_mul_f32 v[40:41], v[46:47], v[8:9]
	global_load_dwordx4 v[6:9], v126, s[0:1]
	s_waitcnt vmcnt(14)
	v_pk_add_f32 v[14:15], v[56:57], 1.0 op_sel_hi:[1,0]
	v_pk_add_f32 v[16:17], v[54:55], 1.0 op_sel_hi:[1,0]
	s_waitcnt vmcnt(13)
	v_pk_mul_f32 v[46:47], v[64:65], v[14:15]
	v_pk_mul_f32 v[48:49], v[62:63], v[16:17]
	s_waitcnt vmcnt(12)
	v_pk_add_f32 v[14:15], v[68:69], 1.0 op_sel_hi:[1,0]
	v_pk_add_f32 v[16:17], v[66:67], 1.0 op_sel_hi:[1,0]
	s_waitcnt vmcnt(11)
	v_pk_mul_f32 v[54:55], v[72:73], v[14:15]
	v_pk_mul_f32 v[56:57], v[70:71], v[16:17]
	global_load_dwordx4 v[14:17], v127, s[0:1]
	s_waitcnt vmcnt(11)
	v_pk_add_f32 v[22:23], v[76:77], 1.0 op_sel_hi:[1,0]
	v_pk_add_f32 v[24:25], v[74:75], 1.0 op_sel_hi:[1,0]
	s_waitcnt vmcnt(10)
	v_pk_mul_f32 v[62:63], v[80:81], v[22:23]
	v_pk_mul_f32 v[64:65], v[78:79], v[24:25]
	global_load_dwordx4 v[22:25], v131, s[0:1]
	s_waitcnt vmcnt(10)
	v_pk_add_f32 v[30:31], v[84:85], 1.0 op_sel_hi:[1,0]
	v_pk_add_f32 v[32:33], v[82:83], 1.0 op_sel_hi:[1,0]
	s_waitcnt vmcnt(9)
	v_pk_mul_f32 v[66:67], v[90:91], v[30:31]
	v_pk_mul_f32 v[68:69], v[88:89], v[32:33]
	global_load_dwordx4 v[30:33], v128, s[0:1]
	v_mul_f32_e32 v74, 0x45800000, v1
	v_cndmask_b32_e32 v74, v1, v74, vcc
	v_pk_mul_f32 v[58:59], v[58:59], v[74:75] op_sel_hi:[1,0]
	v_pk_mul_f32 v[60:61], v[60:61], v[74:75] op_sel_hi:[1,0]
	s_waitcnt vmcnt(7)
	v_pk_fma_f32 v[58:59], v[122:123], v[58:59], v[106:107]
	v_mov_b32_e32 v75, v99
	v_med3_f32 v1, v58, s22, v132
	v_med3_f32 v58, v59, s22, v132
	v_cvt_pk_fp8_f32 v75, v1, v58
	v_pk_fma_f32 v[58:59], v[96:97], v[60:61], v[108:109]
	v_pk_add_f32 v[72:73], v[92:93], 1.0 op_sel_hi:[1,0]
	v_med3_f32 v1, v58, s22, v132
	v_med3_f32 v58, v59, s22, v132
	v_cvt_pk_fp8_f32 v75, v1, v58 op_sel:[0,0,1]
	v_mov_b32_e32 v58, v99
	v_pk_mul_f32 v[72:73], v[102:103], v[72:73]
	v_pk_add_f32 v[70:71], v[94:95], 1.0 op_sel_hi:[1,0]
	v_pk_mul_f32 v[50:51], v[50:51], v[74:75] op_sel_hi:[1,0]
	v_pk_mul_f32 v[52:53], v[52:53], v[74:75] op_sel_hi:[1,0]
	s_waitcnt vmcnt(6)
	v_pk_fma_f32 v[50:51], v[134:135], v[50:51], v[110:111]
	v_pk_mul_f32 v[42:43], v[42:43], v[74:75] op_sel_hi:[1,0]
	v_med3_f32 v1, v50, s22, v132
	v_med3_f32 v50, v51, s22, v132
	v_cvt_pk_fp8_f32 v58, v1, v50
	v_pk_fma_f32 v[50:51], v[124:125], v[52:53], v[112:113]
	s_waitcnt vmcnt(5)
	v_pk_fma_f32 v[40:41], v[40:41], v[42:43], v[114:115]
	v_med3_f32 v1, v50, s22, v132
	v_med3_f32 v50, v51, s22, v132
	v_cvt_pk_fp8_f32 v58, v1, v50 op_sel:[0,0,1]
	v_med3_f32 v1, v40, s22, v132
	v_med3_f32 v40, v41, s22, v132
	v_mov_b32_e32 v41, v99
	v_cvt_pk_fp8_f32 v41, v1, v40
	v_pk_mul_f32 v[44:45], v[44:45], v[74:75] op_sel_hi:[1,0]
	v_pk_mul_f32 v[34:35], v[34:35], v[74:75] op_sel_hi:[1,0]
	v_pk_fma_f32 v[38:39], v[38:39], v[44:45], v[116:117]
	s_waitcnt vmcnt(4)
	v_pk_fma_f32 v[34:35], v[48:49], v[34:35], v[118:119]
	v_med3_f32 v1, v38, s22, v132
	v_med3_f32 v38, v39, s22, v132
	v_cvt_pk_fp8_f32 v41, v1, v38 op_sel:[0,0,1]
	v_med3_f32 v1, v34, s22, v132
	v_med3_f32 v34, v35, s22, v132
	v_mov_b32_e32 v38, v99
	v_cvt_pk_fp8_f32 v38, v1, v34
	v_pk_mul_f32 v[36:37], v[36:37], v[74:75] op_sel_hi:[1,0]
	v_pk_mul_f32 v[26:27], v[26:27], v[74:75] op_sel_hi:[1,0]
	v_pk_fma_f32 v[34:35], v[46:47], v[36:37], v[120:121]
	v_pk_mul_f32 v[28:29], v[28:29], v[74:75] op_sel_hi:[1,0]
	v_med3_f32 v1, v34, s22, v132
	v_med3_f32 v34, v35, s22, v132
	v_cvt_pk_fp8_f32 v38, v1, v34 op_sel:[0,0,1]
	v_pk_mul_f32 v[2:3], v[2:3], v[74:75] op_sel_hi:[1,0]
	v_pk_mul_f32 v[70:71], v[104:105], v[70:71]
	v_pk_mul_f32 v[4:5], v[4:5], v[74:75] op_sel_hi:[1,0]
	s_lshl_b64 s[0:1], s[10:11], 11
	v_lshl_add_u64 v[76:77], v[100:101], 0, s[0:1]
	global_store_dword v[76:77], v75, off
	global_store_dword v[76:77], v58, off offset:256
	global_store_dword v[76:77], v41, off offset:512
	global_store_dword v[76:77], v38, off offset:768
	s_waitcnt vmcnt(7)
	v_pk_fma_f32 v[6:7], v[56:57], v[26:27], v[6:7]
	s_nop 0
	v_med3_f32 v1, v6, s22, v132
	v_med3_f32 v6, v7, s22, v132
	v_mov_b32_e32 v26, v99
	v_cvt_pk_fp8_f32 v26, v1, v6
	v_pk_fma_f32 v[6:7], v[54:55], v[28:29], v[8:9]
	v_pk_mul_f32 v[8:9], v[20:21], v[74:75] op_sel_hi:[1,0]
	v_med3_f32 v1, v6, s22, v132
	v_med3_f32 v6, v7, s22, v132
	v_cvt_pk_fp8_f32 v26, v1, v6 op_sel:[0,0,1]
	v_pk_mul_f32 v[6:7], v[18:19], v[74:75] op_sel_hi:[1,0]
	s_waitcnt vmcnt(4)
	v_pk_fma_f32 v[2:3], v[72:73], v[2:3], v[30:31]
	v_pk_fma_f32 v[6:7], v[64:65], v[6:7], v[14:15]
	v_mov_b32_e32 v14, v99
	v_med3_f32 v1, v6, s22, v132
	v_med3_f32 v6, v7, s22, v132
	v_cvt_pk_fp8_f32 v14, v1, v6
	v_pk_fma_f32 v[6:7], v[62:63], v[8:9], v[16:17]
	v_pk_mul_f32 v[8:9], v[12:13], v[74:75] op_sel_hi:[1,0]
	v_med3_f32 v1, v6, s22, v132
	v_med3_f32 v6, v7, s22, v132
	v_cvt_pk_fp8_f32 v14, v1, v6 op_sel:[0,0,1]
	v_pk_mul_f32 v[6:7], v[10:11], v[74:75] op_sel_hi:[1,0]
	v_mov_b32_e32 v10, v99
	v_pk_fma_f32 v[6:7], v[68:69], v[6:7], v[22:23]
	s_nop 0
	v_med3_f32 v1, v6, s22, v132
	v_med3_f32 v6, v7, s22, v132
	v_cvt_pk_fp8_f32 v10, v1, v6
	v_pk_fma_f32 v[6:7], v[66:67], v[8:9], v[24:25]
	s_nop 0
	v_med3_f32 v1, v6, s22, v132
	v_med3_f32 v6, v7, s22, v132
	v_cvt_pk_fp8_f32 v10, v1, v6 op_sel:[0,0,1]
	v_med3_f32 v1, v2, s22, v132
	v_med3_f32 v2, v3, s22, v132
	v_cvt_pk_fp8_f32 v99, v1, v2
	v_pk_fma_f32 v[2:3], v[70:71], v[4:5], v[32:33]
	s_nop 0
	v_med3_f32 v1, v2, s22, v132
	v_med3_f32 v2, v3, s22, v132
	v_cvt_pk_fp8_f32 v99, v1, v2 op_sel:[0,0,1]
	global_store_dword v[76:77], v26, off offset:1024
	global_store_dword v[76:77], v14, off offset:1280
	global_store_dword v[76:77], v10, off offset:1536
	global_store_dword v[76:77], v99, off offset:1792
